# mLSTM output units: gated output loop unrolled, gain hoisted, all four gate rows requested up front (no wait behind the previous store), sigmoid division without the never-triggered scaling steps
# speedup vs baseline: 1.0119x; 1.0047x over previous
; #define LAS __attribute__((address_space(3)))
; __device__ __forceinline__ bf16_t f2bf(float f) { unsigned u = __builtin_bit_cast(unsigned, f); return (bf16_t)((u + 0x7fffu + ((u >> 16) & 1u)) >> 16); }
; __device__ __forceinline__ int crow(int r, int hi) { return (r & 3) + 8 * (r >> 2) + 4 * hi; }
; __device__ __forceinline__ int crow(int r, int hi) { return (r & 3) + 8 * (r >> 2) + 4 * hi; }
; __device__ __forceinline__ void out_unit_m(LAS unsigned char* lds, LAS unsigned char* ldstab, const OutArgs a, const int wv) {
;     ...
;     __syncthreads();
;     constexpr int TP = DV * 2;
; #pragma unroll
;     for (int r = 0; r < 16; ++r) { const int row = 32 * rb + crow(r, hi);
;         const float inv = rsqrtf((s2[r] + exch[(1 - dh) * 128 + row]) * (1.f / DV) + EPS);
; #pragma unroll
;         for (int nb = 0; nb < 2; ++nb) *(LAS bf16_t*)(lds + row * TP + (dh * 64 + 32 * nb + r32) * 2) = f2bf(o[nb][r] * inv); }
.LBB0_648:
	s_or_b64 exec, exec, s[6:7]
	v_or_b32_e32 v56, s12, v156
	s_lshl_b32 s6, s8, 7
	v_subrev_u32_e32 v48, s6, v56
	s_add_i32 s7, 0, 0x22100
	v_lshl_add_u32 v48, v48, 2, s7
	s_waitcnt lgkmcnt(0)
	s_barrier
	ds_read_b128 v[48:51], v48 offset:512
	v_or_b32_e32 v57, 8, v56
	v_subrev_u32_e32 v52, s6, v57
	v_lshl_add_u32 v52, v52, 2, s7
	ds_read_b128 v[52:55], v52 offset:512
	s_waitcnt lgkmcnt(1)
	v_pk_add_f32 v[48:49], v[44:45], v[48:49]
	v_mov_b64_e32 v[44:45], s[46:47]
	v_pk_fma_f32 v[48:49], v[48:49], s[44:45], v[44:45] op_sel_hi:[1,0,0]
	v_lshlrev_b32_e32 v59, 1, v159
	v_mul_f32_e32 v58, 0x4b800000, v48
	v_cmp_gt_f32_e32 vcc, s83, v48
	s_add_i32 s8, s6, 0
	s_nop 0
	v_cndmask_b32_e32 v48, v48, v58, vcc
	v_rsq_f32_e32 v48, v48
	v_lshlrev_b32_e32 v58, 8, v56
	v_add3_u32 v58, s8, v58, v59
	v_mul_f32_e32 v60, 0x45800000, v48
	v_cndmask_b32_e32 v48, v48, v60, vcc
	v_mul_f32_e32 v0, v0, v48
	v_bfe_u32 v60, v0, 16, 1
	v_add3_u32 v0, v0, v60, s84
	ds_write_b16_d16_hi v58, v0
	v_mul_f32_e32 v0, v16, v48
	v_mul_f32_e32 v16, 0x4b800000, v49
	v_cmp_gt_f32_e32 vcc, s83, v49
	v_bfe_u32 v48, v0, 16, 1
	v_add3_u32 v0, v0, v48, s84
	v_cndmask_b32_e32 v16, v49, v16, vcc
	v_rsq_f32_e32 v16, v16
	ds_write_b16_d16_hi v58, v0 offset:64
	v_mul_f32_e32 v0, 0x45800000, v16
	v_cndmask_b32_e32 v0, v16, v0, vcc
	v_mul_f32_e32 v1, v1, v0
	v_bfe_u32 v16, v1, 16, 1
	v_add3_u32 v1, v1, v16, s84
	ds_write_b16_d16_hi v58, v1 offset:256
	v_mul_f32_e32 v16, v17, v0
	v_pk_add_f32 v[0:1], v[46:47], v[50:51]
	s_nop 0
	v_pk_fma_f32 v[0:1], v[0:1], s[44:45], v[44:45] op_sel_hi:[1,0,0]
	s_nop 0
	v_mul_f32_e32 v17, 0x4b800000, v0
	v_cmp_gt_f32_e32 vcc, s83, v0
	s_nop 1
	v_cndmask_b32_e32 v0, v0, v17, vcc
	v_rsq_f32_e32 v0, v0
	v_bfe_u32 v17, v16, 16, 1
	v_add3_u32 v16, v16, v17, s84
	ds_write_b16_d16_hi v58, v16 offset:320
	v_mul_f32_e32 v16, 0x45800000, v0
	v_cndmask_b32_e32 v0, v0, v16, vcc
	v_mul_f32_e32 v2, v2, v0
	v_bfe_u32 v16, v2, 16, 1
	v_add3_u32 v2, v2, v16, s84
	ds_write_b16_d16_hi v58, v2 offset:512
	v_mul_f32_e32 v2, 0x4b800000, v1
	v_cmp_gt_f32_e32 vcc, s83, v1
	v_mul_f32_e32 v0, v18, v0
	v_or_b32_e32 v17, 16, v56
	v_cndmask_b32_e32 v1, v1, v2, vcc
	v_rsq_f32_e32 v1, v1
	v_bfe_u32 v2, v0, 16, 1
	v_add3_u32 v0, v0, v2, s84
	ds_write_b16_d16_hi v58, v0 offset:576
	v_mul_f32_e32 v0, 0x45800000, v1
	v_cndmask_b32_e32 v0, v1, v0, vcc
	v_mul_f32_e32 v1, v3, v0
	v_bfe_u32 v2, v1, 16, 1
	v_add3_u32 v1, v1, v2, s84
	v_mul_f32_e32 v0, v19, v0
	ds_write_b16_d16_hi v58, v1 offset:768
	v_bfe_u32 v1, v0, 16, 1
	v_add3_u32 v2, v0, v1, s84
	s_waitcnt lgkmcnt(7)
	v_pk_add_f32 v[0:1], v[40:41], v[52:53]
	ds_write_b16_d16_hi v58, v2 offset:832
	v_pk_fma_f32 v[0:1], v[0:1], s[44:45], v[44:45] op_sel_hi:[1,0,0]
	v_lshlrev_b32_e32 v2, 8, v57
	v_mul_f32_e32 v3, 0x4b800000, v0
	v_cmp_gt_f32_e32 vcc, s83, v0
	v_add3_u32 v2, s8, v2, v59
	v_or_b32_e32 v18, 24, v56
	v_cndmask_b32_e32 v0, v0, v3, vcc
	v_rsq_f32_e32 v0, v0
	s_nop 0
	v_mul_f32_e32 v3, 0x45800000, v0
	v_cndmask_b32_e32 v0, v0, v3, vcc
	v_mul_f32_e32 v3, v4, v0
	v_bfe_u32 v4, v3, 16, 1
	v_add3_u32 v3, v3, v4, s84
	ds_write_b16_d16_hi v2, v3
	v_mul_f32_e32 v3, 0x4b800000, v1
	v_cmp_gt_f32_e32 vcc, s83, v1
	v_mul_f32_e32 v0, v20, v0
	v_subrev_u32_e32 v4, s6, v18
	v_cndmask_b32_e32 v1, v1, v3, vcc
	v_rsq_f32_e32 v1, v1
	v_bfe_u32 v3, v0, 16, 1
	v_add3_u32 v0, v0, v3, s84
	ds_write_b16_d16_hi v2, v0 offset:64
	v_mul_f32_e32 v0, 0x45800000, v1
	v_cndmask_b32_e32 v0, v1, v0, vcc
	v_mul_f32_e32 v1, v5, v0
	v_bfe_u32 v2, v1, 16, 1
	v_add3_u32 v1, v1, v2, s84
	ds_write_b16_d16_hi v58, v1 offset:2304
	v_mul_f32_e32 v2, v21, v0
	v_pk_add_f32 v[0:1], v[42:43], v[54:55]
	v_lshl_add_u32 v4, v4, 2, s7
	v_pk_fma_f32 v[0:1], v[0:1], s[44:45], v[44:45] op_sel_hi:[1,0,0]
	s_nop 0
	v_mul_f32_e32 v3, 0x4b800000, v0
	v_cmp_gt_f32_e32 vcc, s83, v0
	s_nop 1
	v_cndmask_b32_e32 v0, v0, v3, vcc
	v_rsq_f32_e32 v0, v0
	v_bfe_u32 v3, v2, 16, 1
	v_add3_u32 v2, v2, v3, s84
	ds_write_b16_d16_hi v58, v2 offset:2368
	v_mul_f32_e32 v2, 0x45800000, v0
	v_cndmask_b32_e32 v0, v0, v2, vcc
	v_mul_f32_e32 v2, v6, v0
	v_bfe_u32 v3, v2, 16, 1
	v_add3_u32 v2, v2, v3, s84
	ds_write_b16_d16_hi v58, v2 offset:2560
	v_mul_f32_e32 v2, 0x4b800000, v1
	v_cmp_gt_f32_e32 vcc, s83, v1
	v_mul_f32_e32 v0, v22, v0
	s_nop 0
	v_cndmask_b32_e32 v1, v1, v2, vcc
	v_rsq_f32_e32 v1, v1
	v_bfe_u32 v2, v0, 16, 1
	v_add3_u32 v0, v0, v2, s84
	ds_write_b16_d16_hi v58, v0 offset:2624
	v_mul_f32_e32 v0, 0x45800000, v1
	v_cndmask_b32_e32 v0, v1, v0, vcc
	v_mul_f32_e32 v1, v7, v0
	v_bfe_u32 v2, v1, 16, 1
	v_add3_u32 v1, v1, v2, s84
	v_mul_f32_e32 v0, v23, v0
	ds_write_b16_d16_hi v58, v1 offset:2816
	v_bfe_u32 v1, v0, 16, 1
	v_add3_u32 v16, v0, v1, s84
	v_subrev_u32_e32 v0, s6, v17
	v_lshl_add_u32 v0, v0, 2, s7
	ds_read_b128 v[0:3], v0 offset:512
	ds_read_b128 v[4:7], v4 offset:512
	ds_write_b16_d16_hi v58, v16 offset:2880
	v_lshlrev_b32_e32 v16, 8, v17
	v_add3_u32 v16, s8, v16, v59
	s_waitcnt lgkmcnt(2)
; #define LAS __attribute__((address_space(3)))
; __device__ __forceinline__ bf16_t f2bf(float f) { unsigned u = __builtin_bit_cast(unsigned, f); return (bf16_t)((u + 0x7fffu + ((u >> 16) & 1u)) >> 16); }
; __device__ __forceinline__ float sigmoidf_(float x) { return 1.f / (1.f + __expf(-x)); }
; __device__ __forceinline__ unsigned pk4_fp8c(float a, float b, float c, float d) { return pk4_fp8(__builtin_amdgcn_fmed3f(a, -448.f, 448.f), __builtin_amdgcn_fmed3f(b, -448.f, 448.f), __builtin_amdgcn_fmed3f(c, -448.f, 448.f), __builtin_amdgcn_fmed3f(d, -448.f, 448.f)); }
; __device__ __forceinline__ int crow(int r, int hi) { return (r & 3) + 8 * (r >> 2) + 4 * hi; }
; __device__ __forceinline__ int crow(int r, int hi) { return (r & 3) + 8 * (r >> 2) + 4 * hi; }
; __device__ __forceinline__ void out_unit_m(LAS unsigned char* lds, LAS unsigned char* ldstab, const OutArgs a, const int wv) {
;     ...
; #pragma unroll
;     for (int r = 0; r < 16; ++r) { const int row = 32 * rb + crow(r, hi);
;         const float inv = rsqrtf((s2[r] + exch[(1 - dh) * 128 + row]) * (1.f / DV) + EPS);
; #pragma unroll
;         for (int nb = 0; nb < 2; ++nb) *(LAS bf16_t*)(lds + row * TP + (dh * 64 + 32 * nb + r32) * 2) = f2bf(o[nb][r] * inv); }
;     __syncthreads();
; #pragma unroll 1
;     for (int id = tid; id < 128 * 16; id += 512) { const int row = id >> 4, ch = id & 15;
;         const u32x4 y = *(const LAS u32x4*)(lds + row * TP + ch * 16); const u32x4 g = *(const u32x4*)(a.G + (size_t)row * a.ldg + 8 * ch);
;         const f32x4 g0 = *(const f32x4*)(a.gain + 8 * ch), g1 = *(const f32x4*)(a.gain + 8 * ch + 4);
;         const float yv[8] = {bf_lo(y.x), bf_hi(y.x), bf_lo(y.y), bf_hi(y.y), bf_lo(y.z), bf_hi(y.z), bf_lo(y.w), bf_hi(y.w)};
;         const float gv[8] = {bf_lo(g.x), bf_hi(g.x), bf_lo(g.y), bf_hi(g.y), bf_lo(g.z), bf_hi(g.z), bf_lo(g.w), bf_hi(g.w)};
;         const float gn[8] = {g0[0], g0[1], g0[2], g0[3], g1[0], g1[1], g1[2], g1[3]};
;         float ov[8];
; #pragma unroll
;         for (int i = 0; i < 8; ++i) ov[i] = yv[i] * gn[i] * sigmoidf_(gv[i]);
;         u32x2 w; w.x = pg8::pk4_fp8c(ov[0] * a.oscale, ov[1] * a.oscale, ov[2] * a.oscale, ov[3] * a.oscale); w.y = pg8::pk4_fp8c(ov[4] * a.oscale, ov[5] * a.oscale, ov[6] * a.oscale, ov[7] * a.oscale);
;         *(u32x2*)(a.Out + (size_t)row * a.ldo + 8 * ch) = w; }
	v_pk_add_f32 v[0:1], v[36:37], v[0:1]
	s_nop 0
	v_pk_fma_f32 v[0:1], v[0:1], s[44:45], v[44:45] op_sel_hi:[1,0,0]
	s_nop 0
	v_mul_f32_e32 v19, 0x4b800000, v0
	v_cmp_gt_f32_e32 vcc, s83, v0
	s_nop 1
	v_cndmask_b32_e32 v0, v0, v19, vcc
	v_rsq_f32_e32 v0, v0
	s_nop 0
	v_mul_f32_e32 v17, 0x45800000, v0
	v_cndmask_b32_e32 v0, v0, v17, vcc
	v_mul_f32_e32 v8, v8, v0
	v_bfe_u32 v17, v8, 16, 1
	v_add3_u32 v8, v8, v17, s84
	ds_write_b16_d16_hi v16, v8
	v_mul_f32_e32 v8, 0x4b800000, v1
	v_cmp_gt_f32_e32 vcc, s83, v1
	v_mul_f32_e32 v0, v24, v0
	s_nop 0
	v_cndmask_b32_e32 v1, v1, v8, vcc
	v_rsq_f32_e32 v1, v1
	v_bfe_u32 v8, v0, 16, 1
	v_add3_u32 v0, v0, v8, s84
	ds_write_b16_d16_hi v16, v0 offset:64
	v_mul_f32_e32 v0, 0x45800000, v1
	v_cndmask_b32_e32 v0, v1, v0, vcc
	v_mul_f32_e32 v1, v9, v0
	v_bfe_u32 v8, v1, 16, 1
	v_add3_u32 v1, v1, v8, s84
	ds_write_b16_d16_hi v58, v1 offset:4352
	v_mul_f32_e32 v8, v25, v0
	v_pk_add_f32 v[0:1], v[38:39], v[2:3]
	s_nop 0
	v_pk_fma_f32 v[0:1], v[0:1], s[44:45], v[44:45] op_sel_hi:[1,0,0]
	s_nop 0
	v_mul_f32_e32 v2, 0x4b800000, v0
	v_cmp_gt_f32_e32 vcc, s83, v0
	s_nop 1
	v_cndmask_b32_e32 v0, v0, v2, vcc
	v_rsq_f32_e32 v0, v0
	v_bfe_u32 v2, v8, 16, 1
	v_add3_u32 v2, v8, v2, s84
	ds_write_b16_d16_hi v58, v2 offset:4416
	v_mul_f32_e32 v2, 0x45800000, v0
	v_cndmask_b32_e32 v0, v0, v2, vcc
	v_mul_f32_e32 v2, v10, v0
	v_bfe_u32 v3, v2, 16, 1
	v_add3_u32 v2, v2, v3, s84
	ds_write_b16_d16_hi v58, v2 offset:4608
	v_mul_f32_e32 v2, 0x4b800000, v1
	v_cmp_gt_f32_e32 vcc, s83, v1
	v_mul_f32_e32 v0, v26, v0
	s_nop 0
	v_cndmask_b32_e32 v1, v1, v2, vcc
	v_rsq_f32_e32 v1, v1
	v_bfe_u32 v2, v0, 16, 1
	v_add3_u32 v0, v0, v2, s84
	ds_write_b16_d16_hi v58, v0 offset:4672
	v_mul_f32_e32 v0, 0x45800000, v1
	v_cndmask_b32_e32 v0, v1, v0, vcc
	v_mul_f32_e32 v1, v11, v0
	v_bfe_u32 v2, v1, 16, 1
	v_add3_u32 v1, v1, v2, s84
	v_mul_f32_e32 v0, v27, v0
	ds_write_b16_d16_hi v58, v1 offset:4864
	v_bfe_u32 v1, v0, 16, 1
	v_add3_u32 v2, v0, v1, s84
	s_waitcnt lgkmcnt(8)
	v_pk_add_f32 v[0:1], v[32:33], v[4:5]
	ds_write_b16_d16_hi v58, v2 offset:4928
	v_pk_fma_f32 v[0:1], v[0:1], s[44:45], v[44:45] op_sel_hi:[1,0,0]
	v_lshlrev_b32_e32 v2, 8, v18
	v_mul_f32_e32 v3, 0x4b800000, v0
	v_cmp_gt_f32_e32 vcc, s83, v0
	v_add3_u32 v2, s8, v2, v59
	s_nop 0
	v_cndmask_b32_e32 v0, v0, v3, vcc
	v_rsq_f32_e32 v0, v0
	s_nop 0
	v_mul_f32_e32 v3, 0x45800000, v0
	v_cndmask_b32_e32 v0, v0, v3, vcc
	v_mul_f32_e32 v3, v12, v0
	v_bfe_u32 v4, v3, 16, 1
	v_add3_u32 v3, v3, v4, s84
	ds_write_b16_d16_hi v2, v3
	v_mul_f32_e32 v3, 0x4b800000, v1
	v_cmp_gt_f32_e32 vcc, s83, v1
	v_mul_f32_e32 v0, v28, v0
	s_nop 0
	v_cndmask_b32_e32 v1, v1, v3, vcc
	v_rsq_f32_e32 v1, v1
	v_bfe_u32 v3, v0, 16, 1
	v_add3_u32 v0, v0, v3, s84
	ds_write_b16_d16_hi v2, v0 offset:64
	v_mul_f32_e32 v0, 0x45800000, v1
	v_cndmask_b32_e32 v0, v1, v0, vcc
	v_mul_f32_e32 v1, v13, v0
	v_bfe_u32 v2, v1, 16, 1
	v_add3_u32 v1, v1, v2, s84
	ds_write_b16_d16_hi v58, v1 offset:6400
	v_mul_f32_e32 v2, v29, v0
	v_pk_add_f32 v[0:1], v[34:35], v[6:7]
	s_nop 0
	v_pk_fma_f32 v[0:1], v[0:1], s[44:45], v[44:45] op_sel_hi:[1,0,0]
	s_nop 0
	v_mul_f32_e32 v3, 0x4b800000, v0
	v_cmp_gt_f32_e32 vcc, s83, v0
	s_nop 1
	v_cndmask_b32_e32 v0, v0, v3, vcc
	v_rsq_f32_e32 v0, v0
	v_bfe_u32 v3, v2, 16, 1
	v_add3_u32 v2, v2, v3, s84
	ds_write_b16_d16_hi v58, v2 offset:6464
	v_mul_f32_e32 v2, 0x45800000, v0
	v_cndmask_b32_e32 v0, v0, v2, vcc
	v_mul_f32_e32 v2, v14, v0
	v_bfe_u32 v3, v2, 16, 1
	v_add3_u32 v2, v2, v3, s84
	ds_write_b16_d16_hi v58, v2 offset:6656
	v_mul_f32_e32 v2, 0x4b800000, v1
	v_cmp_gt_f32_e32 vcc, s83, v1
	v_mul_f32_e32 v0, v30, v0
	s_nop 0
	v_cndmask_b32_e32 v1, v1, v2, vcc
	v_rsq_f32_e32 v1, v1
	v_bfe_u32 v2, v0, 16, 1
	v_add3_u32 v0, v0, v2, s84
	ds_write_b16_d16_hi v58, v0 offset:6720
	v_mul_f32_e32 v0, 0x45800000, v1
	v_cndmask_b32_e32 v0, v1, v0, vcc
	v_mul_f32_e32 v1, v15, v0
	v_bfe_u32 v2, v1, 16, 1
	v_add3_u32 v1, v1, v2, s84
	v_mul_f32_e32 v0, v31, v0
	ds_write_b16_d16_hi v58, v1 offset:6912
	v_bfe_u32 v1, v0, 16, 1
	v_add3_u32 v0, v0, v1, s84
	v_cmp_gt_i32_e32 vcc, s85, v158
	ds_write_b16_d16_hi v58, v0 offset:6976
	s_waitcnt lgkmcnt(0)
	s_barrier
	s_and_saveexec_b64 s[48:49], vcc
	s_cbranch_execz .LBB0_651
	s_lshl_b64 s[6:7], s[40:41], 2
	s_add_u32 s4, s4, s6
	s_addc_u32 s5, s5, s7
	s_add_u32 s6, s65, s89
	s_addc_u32 s7, s66, 0
	s_add_u32 s6, s6, s40
	v_and_b32_e32 v2, 15, v158
	s_addc_u32 s7, s7, 0
	v_lshlrev_b32_e32 v0, 4, v2
	v_lshlrev_b32_e32 v156, 3, v2
	v_mov_b32_e32 v1, v157
	v_lshlrev_b32_e32 v2, 5, v2
	v_mov_b32_e32 v3, v157
	v_add_u32_e32 v8, 0, v0
	v_lshl_add_u64 v[0:1], v[160:161], 0, v[0:1]
	v_lshl_add_u64 v[2:3], s[4:5], 0, v[2:3]
	v_lshl_add_u64 v[4:5], s[6:7], 0, v[156:157]
	s_mov_b64 s[50:51], 0
	v_ashrrev_i32_e32 v6, 4, v158
	global_load_dwordx4 v[36:39], v[2:3], off offset:16
	global_load_dwordx4 v[32:35], v[2:3], off
	v_mad_i64_i32 v[18:19], s[4:5], v6, s71, v[0:1]
	global_load_dwordx4 v[40:43], v[18:19], off offset:3072
	v_add_u32_e32 v9, 32, v6
	v_mad_i64_i32 v[20:21], s[4:5], v9, s71, v[0:1]
	global_load_dwordx4 v[44:47], v[20:21], off offset:3072
	v_add_u32_e32 v9, 64, v6
	v_mad_i64_i32 v[18:19], s[4:5], v9, s71, v[0:1]
	global_load_dwordx4 v[48:51], v[18:19], off offset:3072
	v_add_u32_e32 v9, 96, v6
	v_mad_i64_i32 v[20:21], s[4:5], v9, s71, v[0:1]
	global_load_dwordx4 v[52:55], v[20:21], off offset:3072
	v_lshl_add_u32 v7, v6, 8, v8
	ds_read_b128 v[22:25], v7
	s_waitcnt vmcnt(3) lgkmcnt(0)
; #define LAS __attribute__((address_space(3)))
; __device__ __forceinline__ float sigmoidf_(float x) { return 1.f / (1.f + __expf(-x)); }
; __device__ __forceinline__ unsigned pk4_fp8c(float a, float b, float c, float d) { return pk4_fp8(__builtin_amdgcn_fmed3f(a, -448.f, 448.f), __builtin_amdgcn_fmed3f(b, -448.f, 448.f), __builtin_amdgcn_fmed3f(c, -448.f, 448.f), __builtin_amdgcn_fmed3f(d, -448.f, 448.f)); }
; __device__ __forceinline__ void out_unit_m(LAS unsigned char* lds, LAS unsigned char* ldstab, const OutArgs a, const int wv) {
;     ...
;     for (int id = tid; id < 128 * 16; id += 512) { const int row = id >> 4, ch = id & 15;
;         const u32x4 y = *(const LAS u32x4*)(lds + row * TP + ch * 16); const u32x4 g = *(const u32x4*)(a.G + (size_t)row * a.ldg + 8 * ch);
;         const f32x4 g0 = *(const f32x4*)(a.gain + 8 * ch), g1 = *(const f32x4*)(a.gain + 8 * ch + 4);
;         const float yv[8] = {bf_lo(y.x), bf_hi(y.x), bf_lo(y.y), bf_hi(y.y), bf_lo(y.z), bf_hi(y.z), bf_lo(y.w), bf_hi(y.w)};
;         const float gv[8] = {bf_lo(g.x), bf_hi(g.x), bf_lo(g.y), bf_hi(g.y), bf_lo(g.z), bf_hi(g.z), bf_lo(g.w), bf_hi(g.w)};
;         const float gn[8] = {g0[0], g0[1], g0[2], g0[3], g1[0], g1[1], g1[2], g1[3]};
;         float ov[8];
; #pragma unroll
;         for (int i = 0; i < 8; ++i) ov[i] = yv[i] * gn[i] * sigmoidf_(gv[i]);
;         u32x2 w; w.x = pg8::pk4_fp8c(ov[0] * a.oscale, ov[1] * a.oscale, ov[2] * a.oscale, ov[3] * a.oscale); w.y = pg8::pk4_fp8c(ov[4] * a.oscale, ov[5] * a.oscale, ov[6] * a.oscale, ov[7] * a.oscale);
;         *(u32x2*)(a.Out + (size_t)row * a.ldo + 8 * ch) = w; }
	v_lshlrev_b32_e32 v10, 16, v22
	v_and_b32_e32 v11, 0xffff0000, v22
	v_lshlrev_b32_e32 v12, 16, v23
	v_and_b32_e32 v13, 0xffff0000, v23
	v_lshlrev_b32_e32 v14, 16, v24
	v_and_b32_e32 v15, 0xffff0000, v24
	v_lshlrev_b32_e32 v16, 16, v25
	v_and_b32_e32 v17, 0xffff0000, v25
	v_pk_mul_f32 v[10:11], v[32:33], v[10:11]
	v_pk_mul_f32 v[12:13], v[34:35], v[12:13]
	v_pk_mul_f32 v[14:15], v[36:37], v[14:15]
	v_pk_mul_f32 v[16:17], v[38:39], v[16:17]
	v_lshlrev_b32_e32 v56, 16, v40
	v_and_b32_e32 v57, 0xffff0000, v40
	v_lshlrev_b32_e32 v58, 16, v41
	v_and_b32_e32 v59, 0xffff0000, v41
	v_mul_f32_e32 v56, 0xbfb8aa3b, v56
	v_mul_f32_e32 v57, 0xbfb8aa3b, v57
	v_mul_f32_e32 v58, 0xbfb8aa3b, v58
	v_mul_f32_e32 v59, 0xbfb8aa3b, v59
	v_exp_f32_e32 v56, v56
	v_exp_f32_e32 v57, v57
	v_exp_f32_e32 v58, v58
	v_exp_f32_e32 v59, v59
	v_add_f32_e32 v56, 1.0, v56
	v_add_f32_e32 v57, 1.0, v57
	v_add_f32_e32 v58, 1.0, v58
	v_add_f32_e32 v59, 1.0, v59
	v_rcp_f32_e32 v60, v56
	v_rcp_f32_e32 v61, v57
	v_rcp_f32_e32 v62, v58
	v_rcp_f32_e32 v63, v59
	v_fma_f32 v28, -v56, v60, 1.0
	v_fma_f32 v29, -v57, v61, 1.0
	v_fma_f32 v30, -v58, v62, 1.0
	v_fma_f32 v31, -v59, v63, 1.0
	v_fmac_f32_e32 v60, v28, v60
	v_fmac_f32_e32 v61, v29, v61
	v_fmac_f32_e32 v62, v30, v62
	v_fmac_f32_e32 v63, v31, v63
	v_fma_f32 v28, -v56, v60, 1.0
	v_fma_f32 v29, -v57, v61, 1.0
	v_fma_f32 v30, -v58, v62, 1.0
	v_fma_f32 v31, -v59, v63, 1.0
	v_fma_f32 v64, v28, v60, v60
	v_fma_f32 v65, v29, v61, v61
	v_fma_f32 v66, v30, v62, v62
	v_fma_f32 v67, v31, v63, v63
	v_fma_f32 v28, -v56, v64, 1.0
	v_fma_f32 v29, -v57, v65, 1.0
	v_fma_f32 v30, -v58, v66, 1.0
	v_fma_f32 v31, -v59, v67, 1.0
	v_fma_f32 v28, v28, v60, v64
	v_fma_f32 v29, v29, v61, v65
	v_fma_f32 v30, v30, v62, v66
	v_fma_f32 v31, v31, v63, v67
	v_div_fixup_f32 v28, v28, v56, 1.0
	v_div_fixup_f32 v29, v29, v57, 1.0
	v_div_fixup_f32 v30, v30, v58, 1.0
	v_div_fixup_f32 v31, v31, v59, 1.0
	v_mul_f32_e32 v10, v10, v28
	v_mul_f32_e32 v11, v11, v29
	v_mul_f32_e32 v12, v12, v30
	v_mul_f32_e32 v13, v13, v31
	v_lshlrev_b32_e32 v56, 16, v42
	v_and_b32_e32 v57, 0xffff0000, v42
	v_lshlrev_b32_e32 v58, 16, v43
	v_and_b32_e32 v59, 0xffff0000, v43
	v_mul_f32_e32 v56, 0xbfb8aa3b, v56
	v_mul_f32_e32 v57, 0xbfb8aa3b, v57
	v_mul_f32_e32 v58, 0xbfb8aa3b, v58
	v_mul_f32_e32 v59, 0xbfb8aa3b, v59
	v_exp_f32_e32 v56, v56
	v_exp_f32_e32 v57, v57
	v_exp_f32_e32 v58, v58
	v_exp_f32_e32 v59, v59
	v_add_f32_e32 v56, 1.0, v56
	v_add_f32_e32 v57, 1.0, v57
	v_add_f32_e32 v58, 1.0, v58
	v_add_f32_e32 v59, 1.0, v59
	v_rcp_f32_e32 v60, v56
	v_rcp_f32_e32 v61, v57
	v_rcp_f32_e32 v62, v58
	v_rcp_f32_e32 v63, v59
	v_fma_f32 v28, -v56, v60, 1.0
	v_fma_f32 v29, -v57, v61, 1.0
	v_fma_f32 v30, -v58, v62, 1.0
	v_fma_f32 v31, -v59, v63, 1.0
	v_fmac_f32_e32 v60, v28, v60
	v_fmac_f32_e32 v61, v29, v61
	v_fmac_f32_e32 v62, v30, v62
	v_fmac_f32_e32 v63, v31, v63
	v_fma_f32 v28, -v56, v60, 1.0
	v_fma_f32 v29, -v57, v61, 1.0
	v_fma_f32 v30, -v58, v62, 1.0
	v_fma_f32 v31, -v59, v63, 1.0
	v_fma_f32 v64, v28, v60, v60
	v_fma_f32 v65, v29, v61, v61
	v_fma_f32 v66, v30, v62, v62
	v_fma_f32 v67, v31, v63, v63
	v_fma_f32 v28, -v56, v64, 1.0
	v_fma_f32 v29, -v57, v65, 1.0
	v_fma_f32 v30, -v58, v66, 1.0
	v_fma_f32 v31, -v59, v67, 1.0
	v_fma_f32 v28, v28, v60, v64
	v_fma_f32 v29, v29, v61, v65
	v_fma_f32 v30, v30, v62, v66
	v_fma_f32 v31, v31, v63, v67
	v_div_fixup_f32 v28, v28, v56, 1.0
	v_div_fixup_f32 v29, v29, v57, 1.0
	v_div_fixup_f32 v30, v30, v58, 1.0
	v_div_fixup_f32 v31, v31, v59, 1.0
	v_mul_f32_e32 v14, v14, v28
	v_mul_f32_e32 v15, v15, v29
	v_mul_f32_e32 v16, v16, v30
	v_mul_f32_e32 v17, v17, v31
	v_mul_f32_e32 v10, 0x41800000, v10
	v_mul_f32_e32 v11, 0x41800000, v11
	v_mul_f32_e32 v12, 0x41800000, v12
	v_mul_f32_e32 v13, 0x41800000, v13
	v_mul_f32_e32 v14, 0x41800000, v14
	v_mul_f32_e32 v15, 0x41800000, v15
	v_mul_f32_e32 v16, 0x41800000, v16
	v_mul_f32_e32 v17, 0x41800000, v17
	v_med3_f32 v10, v10, s86, v202
	v_med3_f32 v11, v11, s86, v202
	v_med3_f32 v12, v12, s86, v202
	v_med3_f32 v13, v13, s86, v202
	v_med3_f32 v14, v14, s86, v202
	v_med3_f32 v15, v15, s86, v202
	v_med3_f32 v16, v16, s86, v202
	v_med3_f32 v17, v17, s86, v202
	v_mov_b32_e32 v20, v6
	v_mov_b32_e32 v21, 0
	v_cvt_pk_fp8_f32 v26, v10, v11
	v_cvt_pk_fp8_f32 v27, v14, v15
	v_lshlrev_b64 v[20:21], 10, v[20:21]
	v_cvt_pk_fp8_f32 v26, v12, v13 op_sel:[0,0,1]
	v_cvt_pk_fp8_f32 v27, v16, v17 op_sel:[0,0,1]
	v_lshl_add_u64 v[20:21], v[4:5], 0, v[20:21]
	s_nop 0
	global_store_dwordx2 v[20:21], v[26:27], off
	v_add_u32_e32 v9, 32, v6
	v_lshl_add_u32 v7, v9, 8, v8
	ds_read_b128 v[22:25], v7
	s_waitcnt vmcnt(3) lgkmcnt(0)
; #define LAS __attribute__((address_space(3)))
; __device__ __forceinline__ float sigmoidf_(float x) { return 1.f / (1.f + __expf(-x)); }
; __device__ __forceinline__ unsigned pk4_fp8c(float a, float b, float c, float d) { return pk4_fp8(__builtin_amdgcn_fmed3f(a, -448.f, 448.f), __builtin_amdgcn_fmed3f(b, -448.f, 448.f), __builtin_amdgcn_fmed3f(c, -448.f, 448.f), __builtin_amdgcn_fmed3f(d, -448.f, 448.f)); }
; __device__ __forceinline__ void out_unit_m(LAS unsigned char* lds, LAS unsigned char* ldstab, const OutArgs a, const int wv) {
;     ...
;     for (int id = tid; id < 128 * 16; id += 512) { const int row = id >> 4, ch = id & 15;
;         const u32x4 y = *(const LAS u32x4*)(lds + row * TP + ch * 16); const u32x4 g = *(const u32x4*)(a.G + (size_t)row * a.ldg + 8 * ch);
;         const f32x4 g0 = *(const f32x4*)(a.gain + 8 * ch), g1 = *(const f32x4*)(a.gain + 8 * ch + 4);
;         const float yv[8] = {bf_lo(y.x), bf_hi(y.x), bf_lo(y.y), bf_hi(y.y), bf_lo(y.z), bf_hi(y.z), bf_lo(y.w), bf_hi(y.w)};
;         const float gv[8] = {bf_lo(g.x), bf_hi(g.x), bf_lo(g.y), bf_hi(g.y), bf_lo(g.z), bf_hi(g.z), bf_lo(g.w), bf_hi(g.w)};
;         const float gn[8] = {g0[0], g0[1], g0[2], g0[3], g1[0], g1[1], g1[2], g1[3]};
;         float ov[8];
; #pragma unroll
;         for (int i = 0; i < 8; ++i) ov[i] = yv[i] * gn[i] * sigmoidf_(gv[i]);
;         u32x2 w; w.x = pg8::pk4_fp8c(ov[0] * a.oscale, ov[1] * a.oscale, ov[2] * a.oscale, ov[3] * a.oscale); w.y = pg8::pk4_fp8c(ov[4] * a.oscale, ov[5] * a.oscale, ov[6] * a.oscale, ov[7] * a.oscale);
;         *(u32x2*)(a.Out + (size_t)row * a.ldo + 8 * ch) = w; }
	v_lshlrev_b32_e32 v10, 16, v22
	v_and_b32_e32 v11, 0xffff0000, v22
	v_lshlrev_b32_e32 v12, 16, v23
	v_and_b32_e32 v13, 0xffff0000, v23
	v_lshlrev_b32_e32 v14, 16, v24
	v_and_b32_e32 v15, 0xffff0000, v24
	v_lshlrev_b32_e32 v16, 16, v25
	v_and_b32_e32 v17, 0xffff0000, v25
	v_pk_mul_f32 v[10:11], v[32:33], v[10:11]
	v_pk_mul_f32 v[12:13], v[34:35], v[12:13]
	v_pk_mul_f32 v[14:15], v[36:37], v[14:15]
	v_pk_mul_f32 v[16:17], v[38:39], v[16:17]
	v_lshlrev_b32_e32 v56, 16, v44
	v_and_b32_e32 v57, 0xffff0000, v44
	v_lshlrev_b32_e32 v58, 16, v45
	v_and_b32_e32 v59, 0xffff0000, v45
	v_mul_f32_e32 v56, 0xbfb8aa3b, v56
	v_mul_f32_e32 v57, 0xbfb8aa3b, v57
	v_mul_f32_e32 v58, 0xbfb8aa3b, v58
	v_mul_f32_e32 v59, 0xbfb8aa3b, v59
	v_exp_f32_e32 v56, v56
	v_exp_f32_e32 v57, v57
	v_exp_f32_e32 v58, v58
	v_exp_f32_e32 v59, v59
	v_add_f32_e32 v56, 1.0, v56
	v_add_f32_e32 v57, 1.0, v57
	v_add_f32_e32 v58, 1.0, v58
	v_add_f32_e32 v59, 1.0, v59
	v_rcp_f32_e32 v60, v56
	v_rcp_f32_e32 v61, v57
	v_rcp_f32_e32 v62, v58
	v_rcp_f32_e32 v63, v59
	v_fma_f32 v28, -v56, v60, 1.0
	v_fma_f32 v29, -v57, v61, 1.0
	v_fma_f32 v30, -v58, v62, 1.0
	v_fma_f32 v31, -v59, v63, 1.0
	v_fmac_f32_e32 v60, v28, v60
	v_fmac_f32_e32 v61, v29, v61
	v_fmac_f32_e32 v62, v30, v62
	v_fmac_f32_e32 v63, v31, v63
	v_fma_f32 v28, -v56, v60, 1.0
	v_fma_f32 v29, -v57, v61, 1.0
	v_fma_f32 v30, -v58, v62, 1.0
	v_fma_f32 v31, -v59, v63, 1.0
	v_fma_f32 v64, v28, v60, v60
	v_fma_f32 v65, v29, v61, v61
	v_fma_f32 v66, v30, v62, v62
	v_fma_f32 v67, v31, v63, v63
	v_fma_f32 v28, -v56, v64, 1.0
	v_fma_f32 v29, -v57, v65, 1.0
	v_fma_f32 v30, -v58, v66, 1.0
	v_fma_f32 v31, -v59, v67, 1.0
	v_fma_f32 v28, v28, v60, v64
	v_fma_f32 v29, v29, v61, v65
	v_fma_f32 v30, v30, v62, v66
	v_fma_f32 v31, v31, v63, v67
	v_div_fixup_f32 v28, v28, v56, 1.0
	v_div_fixup_f32 v29, v29, v57, 1.0
	v_div_fixup_f32 v30, v30, v58, 1.0
	v_div_fixup_f32 v31, v31, v59, 1.0
	v_mul_f32_e32 v10, v10, v28
	v_mul_f32_e32 v11, v11, v29
	v_mul_f32_e32 v12, v12, v30
	v_mul_f32_e32 v13, v13, v31
	v_lshlrev_b32_e32 v56, 16, v46
	v_and_b32_e32 v57, 0xffff0000, v46
	v_lshlrev_b32_e32 v58, 16, v47
	v_and_b32_e32 v59, 0xffff0000, v47
	v_mul_f32_e32 v56, 0xbfb8aa3b, v56
	v_mul_f32_e32 v57, 0xbfb8aa3b, v57
	v_mul_f32_e32 v58, 0xbfb8aa3b, v58
	v_mul_f32_e32 v59, 0xbfb8aa3b, v59
	v_exp_f32_e32 v56, v56
	v_exp_f32_e32 v57, v57
	v_exp_f32_e32 v58, v58
	v_exp_f32_e32 v59, v59
	v_add_f32_e32 v56, 1.0, v56
	v_add_f32_e32 v57, 1.0, v57
	v_add_f32_e32 v58, 1.0, v58
	v_add_f32_e32 v59, 1.0, v59
	v_rcp_f32_e32 v60, v56
	v_rcp_f32_e32 v61, v57
	v_rcp_f32_e32 v62, v58
	v_rcp_f32_e32 v63, v59
	v_fma_f32 v28, -v56, v60, 1.0
	v_fma_f32 v29, -v57, v61, 1.0
	v_fma_f32 v30, -v58, v62, 1.0
	v_fma_f32 v31, -v59, v63, 1.0
	v_fmac_f32_e32 v60, v28, v60
	v_fmac_f32_e32 v61, v29, v61
	v_fmac_f32_e32 v62, v30, v62
	v_fmac_f32_e32 v63, v31, v63
	v_fma_f32 v28, -v56, v60, 1.0
	v_fma_f32 v29, -v57, v61, 1.0
	v_fma_f32 v30, -v58, v62, 1.0
	v_fma_f32 v31, -v59, v63, 1.0
	v_fma_f32 v64, v28, v60, v60
	v_fma_f32 v65, v29, v61, v61
	v_fma_f32 v66, v30, v62, v62
	v_fma_f32 v67, v31, v63, v63
	v_fma_f32 v28, -v56, v64, 1.0
	v_fma_f32 v29, -v57, v65, 1.0
	v_fma_f32 v30, -v58, v66, 1.0
	v_fma_f32 v31, -v59, v67, 1.0
	v_fma_f32 v28, v28, v60, v64
	v_fma_f32 v29, v29, v61, v65
	v_fma_f32 v30, v30, v62, v66
	v_fma_f32 v31, v31, v63, v67
	v_div_fixup_f32 v28, v28, v56, 1.0
	v_div_fixup_f32 v29, v29, v57, 1.0
	v_div_fixup_f32 v30, v30, v58, 1.0
	v_div_fixup_f32 v31, v31, v59, 1.0
	v_mul_f32_e32 v14, v14, v28
	v_mul_f32_e32 v15, v15, v29
	v_mul_f32_e32 v16, v16, v30
	v_mul_f32_e32 v17, v17, v31
	v_mul_f32_e32 v10, 0x41800000, v10
	v_mul_f32_e32 v11, 0x41800000, v11
	v_mul_f32_e32 v12, 0x41800000, v12
	v_mul_f32_e32 v13, 0x41800000, v13
	v_mul_f32_e32 v14, 0x41800000, v14
	v_mul_f32_e32 v15, 0x41800000, v15
	v_mul_f32_e32 v16, 0x41800000, v16
	v_mul_f32_e32 v17, 0x41800000, v17
	v_med3_f32 v10, v10, s86, v202
	v_med3_f32 v11, v11, s86, v202
	v_med3_f32 v12, v12, s86, v202
	v_med3_f32 v13, v13, s86, v202
	v_med3_f32 v14, v14, s86, v202
	v_med3_f32 v15, v15, s86, v202
	v_med3_f32 v16, v16, s86, v202
	v_med3_f32 v17, v17, s86, v202
	v_add_u32_e32 v20, 32, v6
	v_mov_b32_e32 v21, 0
	v_cvt_pk_fp8_f32 v26, v10, v11
	v_cvt_pk_fp8_f32 v27, v14, v15
	v_lshlrev_b64 v[20:21], 10, v[20:21]
	v_cvt_pk_fp8_f32 v26, v12, v13 op_sel:[0,0,1]
	v_cvt_pk_fp8_f32 v27, v16, v17 op_sel:[0,0,1]
	v_lshl_add_u64 v[20:21], v[4:5], 0, v[20:21]
	s_nop 0
	global_store_dwordx2 v[20:21], v[26:27], off
	v_add_u32_e32 v9, 64, v6
	v_lshl_add_u32 v7, v9, 8, v8
	ds_read_b128 v[22:25], v7
	s_waitcnt vmcnt(3) lgkmcnt(0)
; #define LAS __attribute__((address_space(3)))
; __device__ __forceinline__ float sigmoidf_(float x) { return 1.f / (1.f + __expf(-x)); }
; __device__ __forceinline__ unsigned pk4_fp8c(float a, float b, float c, float d) { return pk4_fp8(__builtin_amdgcn_fmed3f(a, -448.f, 448.f), __builtin_amdgcn_fmed3f(b, -448.f, 448.f), __builtin_amdgcn_fmed3f(c, -448.f, 448.f), __builtin_amdgcn_fmed3f(d, -448.f, 448.f)); }
; __device__ __forceinline__ void out_unit_m(LAS unsigned char* lds, LAS unsigned char* ldstab, const OutArgs a, const int wv) {
;     ...
;     for (int id = tid; id < 128 * 16; id += 512) { const int row = id >> 4, ch = id & 15;
;         const u32x4 y = *(const LAS u32x4*)(lds + row * TP + ch * 16); const u32x4 g = *(const u32x4*)(a.G + (size_t)row * a.ldg + 8 * ch);
;         const f32x4 g0 = *(const f32x4*)(a.gain + 8 * ch), g1 = *(const f32x4*)(a.gain + 8 * ch + 4);
;         const float yv[8] = {bf_lo(y.x), bf_hi(y.x), bf_lo(y.y), bf_hi(y.y), bf_lo(y.z), bf_hi(y.z), bf_lo(y.w), bf_hi(y.w)};
;         const float gv[8] = {bf_lo(g.x), bf_hi(g.x), bf_lo(g.y), bf_hi(g.y), bf_lo(g.z), bf_hi(g.z), bf_lo(g.w), bf_hi(g.w)};
;         const float gn[8] = {g0[0], g0[1], g0[2], g0[3], g1[0], g1[1], g1[2], g1[3]};
;         float ov[8];
; #pragma unroll
;         for (int i = 0; i < 8; ++i) ov[i] = yv[i] * gn[i] * sigmoidf_(gv[i]);
;         u32x2 w; w.x = pg8::pk4_fp8c(ov[0] * a.oscale, ov[1] * a.oscale, ov[2] * a.oscale, ov[3] * a.oscale); w.y = pg8::pk4_fp8c(ov[4] * a.oscale, ov[5] * a.oscale, ov[6] * a.oscale, ov[7] * a.oscale);
;         *(u32x2*)(a.Out + (size_t)row * a.ldo + 8 * ch) = w; }
	v_lshlrev_b32_e32 v10, 16, v22
	v_and_b32_e32 v11, 0xffff0000, v22
	v_lshlrev_b32_e32 v12, 16, v23
	v_and_b32_e32 v13, 0xffff0000, v23
	v_lshlrev_b32_e32 v14, 16, v24
	v_and_b32_e32 v15, 0xffff0000, v24
	v_lshlrev_b32_e32 v16, 16, v25
	v_and_b32_e32 v17, 0xffff0000, v25
	v_pk_mul_f32 v[10:11], v[32:33], v[10:11]
	v_pk_mul_f32 v[12:13], v[34:35], v[12:13]
	v_pk_mul_f32 v[14:15], v[36:37], v[14:15]
	v_pk_mul_f32 v[16:17], v[38:39], v[16:17]
	v_lshlrev_b32_e32 v56, 16, v48
	v_and_b32_e32 v57, 0xffff0000, v48
	v_lshlrev_b32_e32 v58, 16, v49
	v_and_b32_e32 v59, 0xffff0000, v49
	v_mul_f32_e32 v56, 0xbfb8aa3b, v56
	v_mul_f32_e32 v57, 0xbfb8aa3b, v57
	v_mul_f32_e32 v58, 0xbfb8aa3b, v58
	v_mul_f32_e32 v59, 0xbfb8aa3b, v59
	v_exp_f32_e32 v56, v56
	v_exp_f32_e32 v57, v57
	v_exp_f32_e32 v58, v58
	v_exp_f32_e32 v59, v59
	v_add_f32_e32 v56, 1.0, v56
	v_add_f32_e32 v57, 1.0, v57
	v_add_f32_e32 v58, 1.0, v58
	v_add_f32_e32 v59, 1.0, v59
	v_rcp_f32_e32 v60, v56
	v_rcp_f32_e32 v61, v57
	v_rcp_f32_e32 v62, v58
	v_rcp_f32_e32 v63, v59
	v_fma_f32 v28, -v56, v60, 1.0
	v_fma_f32 v29, -v57, v61, 1.0
	v_fma_f32 v30, -v58, v62, 1.0
	v_fma_f32 v31, -v59, v63, 1.0
	v_fmac_f32_e32 v60, v28, v60
	v_fmac_f32_e32 v61, v29, v61
	v_fmac_f32_e32 v62, v30, v62
	v_fmac_f32_e32 v63, v31, v63
	v_fma_f32 v28, -v56, v60, 1.0
	v_fma_f32 v29, -v57, v61, 1.0
	v_fma_f32 v30, -v58, v62, 1.0
	v_fma_f32 v31, -v59, v63, 1.0
	v_fma_f32 v64, v28, v60, v60
	v_fma_f32 v65, v29, v61, v61
	v_fma_f32 v66, v30, v62, v62
	v_fma_f32 v67, v31, v63, v63
	v_fma_f32 v28, -v56, v64, 1.0
	v_fma_f32 v29, -v57, v65, 1.0
	v_fma_f32 v30, -v58, v66, 1.0
	v_fma_f32 v31, -v59, v67, 1.0
	v_fma_f32 v28, v28, v60, v64
	v_fma_f32 v29, v29, v61, v65
	v_fma_f32 v30, v30, v62, v66
	v_fma_f32 v31, v31, v63, v67
	v_div_fixup_f32 v28, v28, v56, 1.0
	v_div_fixup_f32 v29, v29, v57, 1.0
	v_div_fixup_f32 v30, v30, v58, 1.0
	v_div_fixup_f32 v31, v31, v59, 1.0
	v_mul_f32_e32 v10, v10, v28
	v_mul_f32_e32 v11, v11, v29
	v_mul_f32_e32 v12, v12, v30
	v_mul_f32_e32 v13, v13, v31
	v_lshlrev_b32_e32 v56, 16, v50
	v_and_b32_e32 v57, 0xffff0000, v50
	v_lshlrev_b32_e32 v58, 16, v51
	v_and_b32_e32 v59, 0xffff0000, v51
	v_mul_f32_e32 v56, 0xbfb8aa3b, v56
	v_mul_f32_e32 v57, 0xbfb8aa3b, v57
	v_mul_f32_e32 v58, 0xbfb8aa3b, v58
	v_mul_f32_e32 v59, 0xbfb8aa3b, v59
	v_exp_f32_e32 v56, v56
	v_exp_f32_e32 v57, v57
	v_exp_f32_e32 v58, v58
	v_exp_f32_e32 v59, v59
	v_add_f32_e32 v56, 1.0, v56
	v_add_f32_e32 v57, 1.0, v57
	v_add_f32_e32 v58, 1.0, v58
	v_add_f32_e32 v59, 1.0, v59
	v_rcp_f32_e32 v60, v56
	v_rcp_f32_e32 v61, v57
	v_rcp_f32_e32 v62, v58
	v_rcp_f32_e32 v63, v59
	v_fma_f32 v28, -v56, v60, 1.0
	v_fma_f32 v29, -v57, v61, 1.0
	v_fma_f32 v30, -v58, v62, 1.0
	v_fma_f32 v31, -v59, v63, 1.0
	v_fmac_f32_e32 v60, v28, v60
	v_fmac_f32_e32 v61, v29, v61
	v_fmac_f32_e32 v62, v30, v62
	v_fmac_f32_e32 v63, v31, v63
	v_fma_f32 v28, -v56, v60, 1.0
	v_fma_f32 v29, -v57, v61, 1.0
	v_fma_f32 v30, -v58, v62, 1.0
	v_fma_f32 v31, -v59, v63, 1.0
	v_fma_f32 v64, v28, v60, v60
	v_fma_f32 v65, v29, v61, v61
	v_fma_f32 v66, v30, v62, v62
	v_fma_f32 v67, v31, v63, v63
	v_fma_f32 v28, -v56, v64, 1.0
	v_fma_f32 v29, -v57, v65, 1.0
	v_fma_f32 v30, -v58, v66, 1.0
	v_fma_f32 v31, -v59, v67, 1.0
	v_fma_f32 v28, v28, v60, v64
	v_fma_f32 v29, v29, v61, v65
	v_fma_f32 v30, v30, v62, v66
	v_fma_f32 v31, v31, v63, v67
	v_div_fixup_f32 v28, v28, v56, 1.0
	v_div_fixup_f32 v29, v29, v57, 1.0
	v_div_fixup_f32 v30, v30, v58, 1.0
	v_div_fixup_f32 v31, v31, v59, 1.0
	v_mul_f32_e32 v14, v14, v28
	v_mul_f32_e32 v15, v15, v29
	v_mul_f32_e32 v16, v16, v30
	v_mul_f32_e32 v17, v17, v31
	v_mul_f32_e32 v10, 0x41800000, v10
	v_mul_f32_e32 v11, 0x41800000, v11
	v_mul_f32_e32 v12, 0x41800000, v12
	v_mul_f32_e32 v13, 0x41800000, v13
	v_mul_f32_e32 v14, 0x41800000, v14
	v_mul_f32_e32 v15, 0x41800000, v15
	v_mul_f32_e32 v16, 0x41800000, v16
	v_mul_f32_e32 v17, 0x41800000, v17
	v_med3_f32 v10, v10, s86, v202
	v_med3_f32 v11, v11, s86, v202
	v_med3_f32 v12, v12, s86, v202
	v_med3_f32 v13, v13, s86, v202
	v_med3_f32 v14, v14, s86, v202
	v_med3_f32 v15, v15, s86, v202
	v_med3_f32 v16, v16, s86, v202
	v_med3_f32 v17, v17, s86, v202
	v_add_u32_e32 v20, 64, v6
	v_mov_b32_e32 v21, 0
	v_cvt_pk_fp8_f32 v26, v10, v11
	v_cvt_pk_fp8_f32 v27, v14, v15
	v_lshlrev_b64 v[20:21], 10, v[20:21]
	v_cvt_pk_fp8_f32 v26, v12, v13 op_sel:[0,0,1]
	v_cvt_pk_fp8_f32 v27, v16, v17 op_sel:[0,0,1]
	v_lshl_add_u64 v[20:21], v[4:5], 0, v[20:21]
	s_nop 0
	global_store_dwordx2 v[20:21], v[26:27], off
	v_add_u32_e32 v9, 96, v6
	v_lshl_add_u32 v7, v9, 8, v8
	ds_read_b128 v[22:25], v7
	s_waitcnt vmcnt(3) lgkmcnt(0)
; #define LAS __attribute__((address_space(3)))
; __device__ __forceinline__ float sigmoidf_(float x) { return 1.f / (1.f + __expf(-x)); }
; __device__ __forceinline__ unsigned pk4_fp8c(float a, float b, float c, float d) { return pk4_fp8(__builtin_amdgcn_fmed3f(a, -448.f, 448.f), __builtin_amdgcn_fmed3f(b, -448.f, 448.f), __builtin_amdgcn_fmed3f(c, -448.f, 448.f), __builtin_amdgcn_fmed3f(d, -448.f, 448.f)); }
; __device__ __forceinline__ void out_unit_m(LAS unsigned char* lds, LAS unsigned char* ldstab, const OutArgs a, const int wv) {
;     ...
;     for (int id = tid; id < 128 * 16; id += 512) { const int row = id >> 4, ch = id & 15;
;         const u32x4 y = *(const LAS u32x4*)(lds + row * TP + ch * 16); const u32x4 g = *(const u32x4*)(a.G + (size_t)row * a.ldg + 8 * ch);
;         const f32x4 g0 = *(const f32x4*)(a.gain + 8 * ch), g1 = *(const f32x4*)(a.gain + 8 * ch + 4);
;         const float yv[8] = {bf_lo(y.x), bf_hi(y.x), bf_lo(y.y), bf_hi(y.y), bf_lo(y.z), bf_hi(y.z), bf_lo(y.w), bf_hi(y.w)};
;         const float gv[8] = {bf_lo(g.x), bf_hi(g.x), bf_lo(g.y), bf_hi(g.y), bf_lo(g.z), bf_hi(g.z), bf_lo(g.w), bf_hi(g.w)};
;         const float gn[8] = {g0[0], g0[1], g0[2], g0[3], g1[0], g1[1], g1[2], g1[3]};
;         float ov[8];
; #pragma unroll
;         for (int i = 0; i < 8; ++i) ov[i] = yv[i] * gn[i] * sigmoidf_(gv[i]);
;         u32x2 w; w.x = pg8::pk4_fp8c(ov[0] * a.oscale, ov[1] * a.oscale, ov[2] * a.oscale, ov[3] * a.oscale); w.y = pg8::pk4_fp8c(ov[4] * a.oscale, ov[5] * a.oscale, ov[6] * a.oscale, ov[7] * a.oscale);
;         *(u32x2*)(a.Out + (size_t)row * a.ldo + 8 * ch) = w; }
	v_lshlrev_b32_e32 v10, 16, v22
	v_and_b32_e32 v11, 0xffff0000, v22
	v_lshlrev_b32_e32 v12, 16, v23
	v_and_b32_e32 v13, 0xffff0000, v23
	v_lshlrev_b32_e32 v14, 16, v24
	v_and_b32_e32 v15, 0xffff0000, v24
	v_lshlrev_b32_e32 v16, 16, v25
	v_and_b32_e32 v17, 0xffff0000, v25
	v_pk_mul_f32 v[10:11], v[32:33], v[10:11]
	v_pk_mul_f32 v[12:13], v[34:35], v[12:13]
	v_pk_mul_f32 v[14:15], v[36:37], v[14:15]
	v_pk_mul_f32 v[16:17], v[38:39], v[16:17]
	v_lshlrev_b32_e32 v56, 16, v52
	v_and_b32_e32 v57, 0xffff0000, v52
	v_lshlrev_b32_e32 v58, 16, v53
	v_and_b32_e32 v59, 0xffff0000, v53
	v_mul_f32_e32 v56, 0xbfb8aa3b, v56
	v_mul_f32_e32 v57, 0xbfb8aa3b, v57
	v_mul_f32_e32 v58, 0xbfb8aa3b, v58
	v_mul_f32_e32 v59, 0xbfb8aa3b, v59
	v_exp_f32_e32 v56, v56
	v_exp_f32_e32 v57, v57
	v_exp_f32_e32 v58, v58
	v_exp_f32_e32 v59, v59
	v_add_f32_e32 v56, 1.0, v56
	v_add_f32_e32 v57, 1.0, v57
	v_add_f32_e32 v58, 1.0, v58
	v_add_f32_e32 v59, 1.0, v59
	v_rcp_f32_e32 v60, v56
	v_rcp_f32_e32 v61, v57
	v_rcp_f32_e32 v62, v58
	v_rcp_f32_e32 v63, v59
	v_fma_f32 v28, -v56, v60, 1.0
	v_fma_f32 v29, -v57, v61, 1.0
	v_fma_f32 v30, -v58, v62, 1.0
	v_fma_f32 v31, -v59, v63, 1.0
	v_fmac_f32_e32 v60, v28, v60
	v_fmac_f32_e32 v61, v29, v61
	v_fmac_f32_e32 v62, v30, v62
	v_fmac_f32_e32 v63, v31, v63
	v_fma_f32 v28, -v56, v60, 1.0
	v_fma_f32 v29, -v57, v61, 1.0
	v_fma_f32 v30, -v58, v62, 1.0
	v_fma_f32 v31, -v59, v63, 1.0
	v_fma_f32 v64, v28, v60, v60
	v_fma_f32 v65, v29, v61, v61
	v_fma_f32 v66, v30, v62, v62
	v_fma_f32 v67, v31, v63, v63
	v_fma_f32 v28, -v56, v64, 1.0
	v_fma_f32 v29, -v57, v65, 1.0
	v_fma_f32 v30, -v58, v66, 1.0
	v_fma_f32 v31, -v59, v67, 1.0
	v_fma_f32 v28, v28, v60, v64
	v_fma_f32 v29, v29, v61, v65
	v_fma_f32 v30, v30, v62, v66
	v_fma_f32 v31, v31, v63, v67
	v_div_fixup_f32 v28, v28, v56, 1.0
	v_div_fixup_f32 v29, v29, v57, 1.0
	v_div_fixup_f32 v30, v30, v58, 1.0
	v_div_fixup_f32 v31, v31, v59, 1.0
	v_mul_f32_e32 v10, v10, v28
	v_mul_f32_e32 v11, v11, v29
	v_mul_f32_e32 v12, v12, v30
	v_mul_f32_e32 v13, v13, v31
	v_lshlrev_b32_e32 v56, 16, v54
	v_and_b32_e32 v57, 0xffff0000, v54
	v_lshlrev_b32_e32 v58, 16, v55
	v_and_b32_e32 v59, 0xffff0000, v55
	v_mul_f32_e32 v56, 0xbfb8aa3b, v56
	v_mul_f32_e32 v57, 0xbfb8aa3b, v57
	v_mul_f32_e32 v58, 0xbfb8aa3b, v58
	v_mul_f32_e32 v59, 0xbfb8aa3b, v59
	v_exp_f32_e32 v56, v56
	v_exp_f32_e32 v57, v57
	v_exp_f32_e32 v58, v58
	v_exp_f32_e32 v59, v59
	v_add_f32_e32 v56, 1.0, v56
	v_add_f32_e32 v57, 1.0, v57
	v_add_f32_e32 v58, 1.0, v58
	v_add_f32_e32 v59, 1.0, v59
	v_rcp_f32_e32 v60, v56
	v_rcp_f32_e32 v61, v57
	v_rcp_f32_e32 v62, v58
	v_rcp_f32_e32 v63, v59
	v_fma_f32 v28, -v56, v60, 1.0
	v_fma_f32 v29, -v57, v61, 1.0
	v_fma_f32 v30, -v58, v62, 1.0
	v_fma_f32 v31, -v59, v63, 1.0
	v_fmac_f32_e32 v60, v28, v60
	v_fmac_f32_e32 v61, v29, v61
	v_fmac_f32_e32 v62, v30, v62
	v_fmac_f32_e32 v63, v31, v63
	v_fma_f32 v28, -v56, v60, 1.0
	v_fma_f32 v29, -v57, v61, 1.0
	v_fma_f32 v30, -v58, v62, 1.0
	v_fma_f32 v31, -v59, v63, 1.0
	v_fma_f32 v64, v28, v60, v60
	v_fma_f32 v65, v29, v61, v61
	v_fma_f32 v66, v30, v62, v62
	v_fma_f32 v67, v31, v63, v63
	v_fma_f32 v28, -v56, v64, 1.0
	v_fma_f32 v29, -v57, v65, 1.0
	v_fma_f32 v30, -v58, v66, 1.0
	v_fma_f32 v31, -v59, v67, 1.0
	v_fma_f32 v28, v28, v60, v64
	v_fma_f32 v29, v29, v61, v65
	v_fma_f32 v30, v30, v62, v66
	v_fma_f32 v31, v31, v63, v67
	v_div_fixup_f32 v28, v28, v56, 1.0
	v_div_fixup_f32 v29, v29, v57, 1.0
	v_div_fixup_f32 v30, v30, v58, 1.0
	v_div_fixup_f32 v31, v31, v59, 1.0
	v_mul_f32_e32 v14, v14, v28
	v_mul_f32_e32 v15, v15, v29
	v_mul_f32_e32 v16, v16, v30
	v_mul_f32_e32 v17, v17, v31
	v_mul_f32_e32 v10, 0x41800000, v10
	v_mul_f32_e32 v11, 0x41800000, v11
	v_mul_f32_e32 v12, 0x41800000, v12
	v_mul_f32_e32 v13, 0x41800000, v13
	v_mul_f32_e32 v14, 0x41800000, v14
	v_mul_f32_e32 v15, 0x41800000, v15
	v_mul_f32_e32 v16, 0x41800000, v16
	v_mul_f32_e32 v17, 0x41800000, v17
	v_med3_f32 v10, v10, s86, v202
	v_med3_f32 v11, v11, s86, v202
	v_med3_f32 v12, v12, s86, v202
	v_med3_f32 v13, v13, s86, v202
	v_med3_f32 v14, v14, s86, v202
	v_med3_f32 v15, v15, s86, v202
	v_med3_f32 v16, v16, s86, v202
	v_med3_f32 v17, v17, s86, v202
	v_add_u32_e32 v20, 96, v6
	v_mov_b32_e32 v21, 0
	v_cvt_pk_fp8_f32 v26, v10, v11
	v_cvt_pk_fp8_f32 v27, v14, v15
	v_lshlrev_b64 v[20:21], 10, v[20:21]
	v_cvt_pk_fp8_f32 v26, v12, v13 op_sel:[0,0,1]
	v_cvt_pk_fp8_f32 v27, v16, v17 op_sel:[0,0,1]
	v_lshl_add_u64 v[20:21], v[4:5], 0, v[20:21]
	s_nop 0
	global_store_dwordx2 v[20:21], v[26:27], off

; #define LAS __attribute__((address_space(3)))
; __device__ __forceinline__ bf16_t f2bf(float f) { unsigned u = __builtin_bit_cast(unsigned, f); return (bf16_t)((u + 0x7fffu + ((u >> 16) & 1u)) >> 16); }
; __device__ __forceinline__ int crow(int r, int hi) { return (r & 3) + 8 * (r >> 2) + 4 * hi; }
; __device__ __forceinline__ int crow(int r, int hi) { return (r & 3) + 8 * (r >> 2) + 4 * hi; }
; __device__ __forceinline__ void out_unit_m(LAS unsigned char* lds, LAS unsigned char* ldstab, const OutArgs a, const int wv) {
;     ...
;     __syncthreads();
;     constexpr int TP = DV * 2;
; #pragma unroll
;     for (int r = 0; r < 16; ++r) { const int row = 32 * rb + crow(r, hi);
;         const float inv = rsqrtf((s2[r] + exch[(1 - dh) * 128 + row]) * (1.f / DV) + EPS);
; #pragma unroll
;         for (int nb = 0; nb < 2; ++nb) *(LAS bf16_t*)(lds + row * TP + (dh * 64 + 32 * nb + r32) * 2) = f2bf(o[nb][r] * inv); }
.LBB0_3189:
	s_or_b64 exec, exec, s[6:7]
	v_or_b32_e32 v56, s12, v156
	s_lshl_b32 s6, s8, 7
	v_subrev_u32_e32 v48, s6, v56
	s_add_i32 s7, 0, 0x22100
	v_lshl_add_u32 v48, v48, 2, s7
	s_waitcnt lgkmcnt(0)
	s_barrier
	ds_read_b128 v[48:51], v48 offset:512
	v_or_b32_e32 v57, 8, v56
	v_subrev_u32_e32 v52, s6, v57
	v_lshl_add_u32 v52, v52, 2, s7
	ds_read_b128 v[52:55], v52 offset:512
	s_waitcnt lgkmcnt(1)
	v_pk_add_f32 v[48:49], v[44:45], v[48:49]
	v_mov_b64_e32 v[44:45], s[46:47]
	v_pk_fma_f32 v[48:49], v[48:49], s[44:45], v[44:45] op_sel_hi:[1,0,0]
	v_lshlrev_b32_e32 v59, 1, v159
	v_mul_f32_e32 v58, 0x4b800000, v48
	v_cmp_gt_f32_e32 vcc, s83, v48
	s_add_i32 s8, s6, 0
	s_nop 0
	v_cndmask_b32_e32 v48, v48, v58, vcc
	v_rsq_f32_e32 v48, v48
	v_lshlrev_b32_e32 v58, 8, v56
	v_add3_u32 v58, s8, v58, v59
	v_mul_f32_e32 v60, 0x45800000, v48
	v_cndmask_b32_e32 v48, v48, v60, vcc
	v_mul_f32_e32 v0, v0, v48
	v_bfe_u32 v60, v0, 16, 1
	v_add3_u32 v0, v0, v60, s84
	ds_write_b16_d16_hi v58, v0
	v_mul_f32_e32 v0, v16, v48
	v_mul_f32_e32 v16, 0x4b800000, v49
	v_cmp_gt_f32_e32 vcc, s83, v49
	v_bfe_u32 v48, v0, 16, 1
	v_add3_u32 v0, v0, v48, s84
	v_cndmask_b32_e32 v16, v49, v16, vcc
	v_rsq_f32_e32 v16, v16
	ds_write_b16_d16_hi v58, v0 offset:64
	v_mul_f32_e32 v0, 0x45800000, v16
	v_cndmask_b32_e32 v0, v16, v0, vcc
	v_mul_f32_e32 v1, v1, v0
	v_bfe_u32 v16, v1, 16, 1
	v_add3_u32 v1, v1, v16, s84
	ds_write_b16_d16_hi v58, v1 offset:256
	v_mul_f32_e32 v16, v17, v0
	v_pk_add_f32 v[0:1], v[46:47], v[50:51]
	s_nop 0
	v_pk_fma_f32 v[0:1], v[0:1], s[44:45], v[44:45] op_sel_hi:[1,0,0]
	s_nop 0
	v_mul_f32_e32 v17, 0x4b800000, v0
	v_cmp_gt_f32_e32 vcc, s83, v0
	s_nop 1
	v_cndmask_b32_e32 v0, v0, v17, vcc
	v_rsq_f32_e32 v0, v0
	v_bfe_u32 v17, v16, 16, 1
	v_add3_u32 v16, v16, v17, s84
	ds_write_b16_d16_hi v58, v16 offset:320
	v_mul_f32_e32 v16, 0x45800000, v0
	v_cndmask_b32_e32 v0, v0, v16, vcc
	v_mul_f32_e32 v2, v2, v0
	v_bfe_u32 v16, v2, 16, 1
	v_add3_u32 v2, v2, v16, s84
	ds_write_b16_d16_hi v58, v2 offset:512
	v_mul_f32_e32 v2, 0x4b800000, v1
	v_cmp_gt_f32_e32 vcc, s83, v1
	v_mul_f32_e32 v0, v18, v0
	v_or_b32_e32 v17, 16, v56
	v_cndmask_b32_e32 v1, v1, v2, vcc
	v_rsq_f32_e32 v1, v1
	v_bfe_u32 v2, v0, 16, 1
	v_add3_u32 v0, v0, v2, s84
	ds_write_b16_d16_hi v58, v0 offset:576
	v_mul_f32_e32 v0, 0x45800000, v1
	v_cndmask_b32_e32 v0, v1, v0, vcc
	v_mul_f32_e32 v1, v3, v0
	v_bfe_u32 v2, v1, 16, 1
	v_add3_u32 v1, v1, v2, s84
	v_mul_f32_e32 v0, v19, v0
	ds_write_b16_d16_hi v58, v1 offset:768
	v_bfe_u32 v1, v0, 16, 1
	v_add3_u32 v2, v0, v1, s84
	s_waitcnt lgkmcnt(7)
	v_pk_add_f32 v[0:1], v[40:41], v[52:53]
	ds_write_b16_d16_hi v58, v2 offset:832
	v_pk_fma_f32 v[0:1], v[0:1], s[44:45], v[44:45] op_sel_hi:[1,0,0]
	v_lshlrev_b32_e32 v2, 8, v57
	v_mul_f32_e32 v3, 0x4b800000, v0
	v_cmp_gt_f32_e32 vcc, s83, v0
	v_add3_u32 v2, s8, v2, v59
	v_or_b32_e32 v18, 24, v56
	v_cndmask_b32_e32 v0, v0, v3, vcc
	v_rsq_f32_e32 v0, v0
	s_nop 0
	v_mul_f32_e32 v3, 0x45800000, v0
	v_cndmask_b32_e32 v0, v0, v3, vcc
	v_mul_f32_e32 v3, v4, v0
	v_bfe_u32 v4, v3, 16, 1
	v_add3_u32 v3, v3, v4, s84
	ds_write_b16_d16_hi v2, v3
	v_mul_f32_e32 v3, 0x4b800000, v1
	v_cmp_gt_f32_e32 vcc, s83, v1
	v_mul_f32_e32 v0, v20, v0
	v_subrev_u32_e32 v4, s6, v18
	v_cndmask_b32_e32 v1, v1, v3, vcc
	v_rsq_f32_e32 v1, v1
	v_bfe_u32 v3, v0, 16, 1
	v_add3_u32 v0, v0, v3, s84
	ds_write_b16_d16_hi v2, v0 offset:64
	v_mul_f32_e32 v0, 0x45800000, v1
	v_cndmask_b32_e32 v0, v1, v0, vcc
	v_mul_f32_e32 v1, v5, v0
	v_bfe_u32 v2, v1, 16, 1
	v_add3_u32 v1, v1, v2, s84
	ds_write_b16_d16_hi v58, v1 offset:2304
	v_mul_f32_e32 v2, v21, v0
	v_pk_add_f32 v[0:1], v[42:43], v[54:55]
	v_lshl_add_u32 v4, v4, 2, s7
	v_pk_fma_f32 v[0:1], v[0:1], s[44:45], v[44:45] op_sel_hi:[1,0,0]
	s_nop 0
	v_mul_f32_e32 v3, 0x4b800000, v0
	v_cmp_gt_f32_e32 vcc, s83, v0
	s_nop 1
	v_cndmask_b32_e32 v0, v0, v3, vcc
	v_rsq_f32_e32 v0, v0
	v_bfe_u32 v3, v2, 16, 1
	v_add3_u32 v2, v2, v3, s84
	ds_write_b16_d16_hi v58, v2 offset:2368
	v_mul_f32_e32 v2, 0x45800000, v0
	v_cndmask_b32_e32 v0, v0, v2, vcc
	v_mul_f32_e32 v2, v6, v0
	v_bfe_u32 v3, v2, 16, 1
	v_add3_u32 v2, v2, v3, s84
	ds_write_b16_d16_hi v58, v2 offset:2560
	v_mul_f32_e32 v2, 0x4b800000, v1
	v_cmp_gt_f32_e32 vcc, s83, v1
	v_mul_f32_e32 v0, v22, v0
	s_nop 0
	v_cndmask_b32_e32 v1, v1, v2, vcc
	v_rsq_f32_e32 v1, v1
	v_bfe_u32 v2, v0, 16, 1
	v_add3_u32 v0, v0, v2, s84
	ds_write_b16_d16_hi v58, v0 offset:2624
	v_mul_f32_e32 v0, 0x45800000, v1
	v_cndmask_b32_e32 v0, v1, v0, vcc
	v_mul_f32_e32 v1, v7, v0
	v_bfe_u32 v2, v1, 16, 1
	v_add3_u32 v1, v1, v2, s84
	v_mul_f32_e32 v0, v23, v0
	ds_write_b16_d16_hi v58, v1 offset:2816
	v_bfe_u32 v1, v0, 16, 1
	v_add3_u32 v16, v0, v1, s84
	v_subrev_u32_e32 v0, s6, v17
	v_lshl_add_u32 v0, v0, 2, s7
	ds_read_b128 v[0:3], v0 offset:512
	ds_read_b128 v[4:7], v4 offset:512
	ds_write_b16_d16_hi v58, v16 offset:2880
	v_lshlrev_b32_e32 v16, 8, v17
	v_add3_u32 v16, s8, v16, v59
	s_waitcnt lgkmcnt(2)
; #define LAS __attribute__((address_space(3)))
; __device__ __forceinline__ bf16_t f2bf(float f) { unsigned u = __builtin_bit_cast(unsigned, f); return (bf16_t)((u + 0x7fffu + ((u >> 16) & 1u)) >> 16); }
; __device__ __forceinline__ float sigmoidf_(float x) { return 1.f / (1.f + __expf(-x)); }
; __device__ __forceinline__ unsigned pk4_fp8c(float a, float b, float c, float d) { return pk4_fp8(__builtin_amdgcn_fmed3f(a, -448.f, 448.f), __builtin_amdgcn_fmed3f(b, -448.f, 448.f), __builtin_amdgcn_fmed3f(c, -448.f, 448.f), __builtin_amdgcn_fmed3f(d, -448.f, 448.f)); }
; __device__ __forceinline__ int crow(int r, int hi) { return (r & 3) + 8 * (r >> 2) + 4 * hi; }
; __device__ __forceinline__ int crow(int r, int hi) { return (r & 3) + 8 * (r >> 2) + 4 * hi; }
; __device__ __forceinline__ void out_unit_m(LAS unsigned char* lds, LAS unsigned char* ldstab, const OutArgs a, const int wv) {
;     ...
; #pragma unroll
;     for (int r = 0; r < 16; ++r) { const int row = 32 * rb + crow(r, hi);
;         const float inv = rsqrtf((s2[r] + exch[(1 - dh) * 128 + row]) * (1.f / DV) + EPS);
; #pragma unroll
;         for (int nb = 0; nb < 2; ++nb) *(LAS bf16_t*)(lds + row * TP + (dh * 64 + 32 * nb + r32) * 2) = f2bf(o[nb][r] * inv); }
;     __syncthreads();
; #pragma unroll 1
;     for (int id = tid; id < 128 * 16; id += 512) { const int row = id >> 4, ch = id & 15;
;         const u32x4 y = *(const LAS u32x4*)(lds + row * TP + ch * 16); const u32x4 g = *(const u32x4*)(a.G + (size_t)row * a.ldg + 8 * ch);
;         const f32x4 g0 = *(const f32x4*)(a.gain + 8 * ch), g1 = *(const f32x4*)(a.gain + 8 * ch + 4);
;         const float yv[8] = {bf_lo(y.x), bf_hi(y.x), bf_lo(y.y), bf_hi(y.y), bf_lo(y.z), bf_hi(y.z), bf_lo(y.w), bf_hi(y.w)};
;         const float gv[8] = {bf_lo(g.x), bf_hi(g.x), bf_lo(g.y), bf_hi(g.y), bf_lo(g.z), bf_hi(g.z), bf_lo(g.w), bf_hi(g.w)};
;         const float gn[8] = {g0[0], g0[1], g0[2], g0[3], g1[0], g1[1], g1[2], g1[3]};
;         float ov[8];
; #pragma unroll
;         for (int i = 0; i < 8; ++i) ov[i] = yv[i] * gn[i] * sigmoidf_(gv[i]);
;         u32x2 w; w.x = pg8::pk4_fp8c(ov[0] * a.oscale, ov[1] * a.oscale, ov[2] * a.oscale, ov[3] * a.oscale); w.y = pg8::pk4_fp8c(ov[4] * a.oscale, ov[5] * a.oscale, ov[6] * a.oscale, ov[7] * a.oscale);
;         *(u32x2*)(a.Out + (size_t)row * a.ldo + 8 * ch) = w; }
	v_pk_add_f32 v[0:1], v[36:37], v[0:1]
	s_nop 0
	v_pk_fma_f32 v[0:1], v[0:1], s[44:45], v[44:45] op_sel_hi:[1,0,0]
	s_nop 0
	v_mul_f32_e32 v19, 0x4b800000, v0
	v_cmp_gt_f32_e32 vcc, s83, v0
	s_nop 1
	v_cndmask_b32_e32 v0, v0, v19, vcc
	v_rsq_f32_e32 v0, v0
	s_nop 0
	v_mul_f32_e32 v17, 0x45800000, v0
	v_cndmask_b32_e32 v0, v0, v17, vcc
	v_mul_f32_e32 v8, v8, v0
	v_bfe_u32 v17, v8, 16, 1
	v_add3_u32 v8, v8, v17, s84
	ds_write_b16_d16_hi v16, v8
	v_mul_f32_e32 v8, 0x4b800000, v1
	v_cmp_gt_f32_e32 vcc, s83, v1
	v_mul_f32_e32 v0, v24, v0
	s_nop 0
	v_cndmask_b32_e32 v1, v1, v8, vcc
	v_rsq_f32_e32 v1, v1
	v_bfe_u32 v8, v0, 16, 1
	v_add3_u32 v0, v0, v8, s84
	ds_write_b16_d16_hi v16, v0 offset:64
	v_mul_f32_e32 v0, 0x45800000, v1
	v_cndmask_b32_e32 v0, v1, v0, vcc
	v_mul_f32_e32 v1, v9, v0
	v_bfe_u32 v8, v1, 16, 1
	v_add3_u32 v1, v1, v8, s84
	ds_write_b16_d16_hi v58, v1 offset:4352
	v_mul_f32_e32 v8, v25, v0
	v_pk_add_f32 v[0:1], v[38:39], v[2:3]
	s_nop 0
	v_pk_fma_f32 v[0:1], v[0:1], s[44:45], v[44:45] op_sel_hi:[1,0,0]
	s_nop 0
	v_mul_f32_e32 v2, 0x4b800000, v0
	v_cmp_gt_f32_e32 vcc, s83, v0
	s_nop 1
	v_cndmask_b32_e32 v0, v0, v2, vcc
	v_rsq_f32_e32 v0, v0
	v_bfe_u32 v2, v8, 16, 1
	v_add3_u32 v2, v8, v2, s84
	ds_write_b16_d16_hi v58, v2 offset:4416
	v_mul_f32_e32 v2, 0x45800000, v0
	v_cndmask_b32_e32 v0, v0, v2, vcc
	v_mul_f32_e32 v2, v10, v0
	v_bfe_u32 v3, v2, 16, 1
	v_add3_u32 v2, v2, v3, s84
	ds_write_b16_d16_hi v58, v2 offset:4608
	v_mul_f32_e32 v2, 0x4b800000, v1
	v_cmp_gt_f32_e32 vcc, s83, v1
	v_mul_f32_e32 v0, v26, v0
	s_nop 0
	v_cndmask_b32_e32 v1, v1, v2, vcc
	v_rsq_f32_e32 v1, v1
	v_bfe_u32 v2, v0, 16, 1
	v_add3_u32 v0, v0, v2, s84
	ds_write_b16_d16_hi v58, v0 offset:4672
	v_mul_f32_e32 v0, 0x45800000, v1
	v_cndmask_b32_e32 v0, v1, v0, vcc
	v_mul_f32_e32 v1, v11, v0
	v_bfe_u32 v2, v1, 16, 1
	v_add3_u32 v1, v1, v2, s84
	v_mul_f32_e32 v0, v27, v0
	ds_write_b16_d16_hi v58, v1 offset:4864
	v_bfe_u32 v1, v0, 16, 1
	v_add3_u32 v2, v0, v1, s84
	s_waitcnt lgkmcnt(8)
	v_pk_add_f32 v[0:1], v[32:33], v[4:5]
	ds_write_b16_d16_hi v58, v2 offset:4928
	v_pk_fma_f32 v[0:1], v[0:1], s[44:45], v[44:45] op_sel_hi:[1,0,0]
	v_lshlrev_b32_e32 v2, 8, v18
	v_mul_f32_e32 v3, 0x4b800000, v0
	v_cmp_gt_f32_e32 vcc, s83, v0
	v_add3_u32 v2, s8, v2, v59
	s_nop 0
	v_cndmask_b32_e32 v0, v0, v3, vcc
	v_rsq_f32_e32 v0, v0
	s_nop 0
	v_mul_f32_e32 v3, 0x45800000, v0
	v_cndmask_b32_e32 v0, v0, v3, vcc
	v_mul_f32_e32 v3, v12, v0
	v_bfe_u32 v4, v3, 16, 1
	v_add3_u32 v3, v3, v4, s84
	ds_write_b16_d16_hi v2, v3
	v_mul_f32_e32 v3, 0x4b800000, v1
	v_cmp_gt_f32_e32 vcc, s83, v1
	v_mul_f32_e32 v0, v28, v0
	s_nop 0
	v_cndmask_b32_e32 v1, v1, v3, vcc
	v_rsq_f32_e32 v1, v1
	v_bfe_u32 v3, v0, 16, 1
	v_add3_u32 v0, v0, v3, s84
	ds_write_b16_d16_hi v2, v0 offset:64
	v_mul_f32_e32 v0, 0x45800000, v1
	v_cndmask_b32_e32 v0, v1, v0, vcc
	v_mul_f32_e32 v1, v13, v0
	v_bfe_u32 v2, v1, 16, 1
	v_add3_u32 v1, v1, v2, s84
	ds_write_b16_d16_hi v58, v1 offset:6400
	v_mul_f32_e32 v2, v29, v0
	v_pk_add_f32 v[0:1], v[34:35], v[6:7]
	s_nop 0
	v_pk_fma_f32 v[0:1], v[0:1], s[44:45], v[44:45] op_sel_hi:[1,0,0]
	s_nop 0
	v_mul_f32_e32 v3, 0x4b800000, v0
	v_cmp_gt_f32_e32 vcc, s83, v0
	s_nop 1
	v_cndmask_b32_e32 v0, v0, v3, vcc
	v_rsq_f32_e32 v0, v0
	v_bfe_u32 v3, v2, 16, 1
	v_add3_u32 v2, v2, v3, s84
	ds_write_b16_d16_hi v58, v2 offset:6464
	v_mul_f32_e32 v2, 0x45800000, v0
	v_cndmask_b32_e32 v0, v0, v2, vcc
	v_mul_f32_e32 v2, v14, v0
	v_bfe_u32 v3, v2, 16, 1
	v_add3_u32 v2, v2, v3, s84
	ds_write_b16_d16_hi v58, v2 offset:6656
	v_mul_f32_e32 v2, 0x4b800000, v1
	v_cmp_gt_f32_e32 vcc, s83, v1
	v_mul_f32_e32 v0, v30, v0
	s_nop 0
	v_cndmask_b32_e32 v1, v1, v2, vcc
	v_rsq_f32_e32 v1, v1
	v_bfe_u32 v2, v0, 16, 1
	v_add3_u32 v0, v0, v2, s84
	ds_write_b16_d16_hi v58, v0 offset:6720
	v_mul_f32_e32 v0, 0x45800000, v1
	v_cndmask_b32_e32 v0, v1, v0, vcc
	v_mul_f32_e32 v1, v15, v0
	v_bfe_u32 v2, v1, 16, 1
	v_add3_u32 v1, v1, v2, s84
	v_mul_f32_e32 v0, v31, v0
	ds_write_b16_d16_hi v58, v1 offset:6912
	v_bfe_u32 v1, v0, 16, 1
	v_add3_u32 v0, v0, v1, s84
	v_cmp_gt_i32_e32 vcc, s85, v158
	ds_write_b16_d16_hi v58, v0 offset:6976
	s_waitcnt lgkmcnt(0)
	s_barrier
	s_and_saveexec_b64 s[48:49], vcc
	s_cbranch_execz .LBB0_3192
	s_lshl_b64 s[6:7], s[40:41], 2
	s_add_u32 s4, s4, s6
	s_addc_u32 s5, s5, s7
	s_add_u32 s6, s65, s89
	s_addc_u32 s7, s66, 0
	s_add_u32 s6, s6, s40
	v_and_b32_e32 v2, 15, v158
	s_addc_u32 s7, s7, 0
	v_lshlrev_b32_e32 v0, 4, v2
	v_lshlrev_b32_e32 v156, 3, v2
	v_mov_b32_e32 v1, v157
	v_lshlrev_b32_e32 v2, 5, v2
	v_mov_b32_e32 v3, v157
	v_add_u32_e32 v8, 0, v0
	v_lshl_add_u64 v[0:1], v[160:161], 0, v[0:1]
	v_lshl_add_u64 v[2:3], s[4:5], 0, v[2:3]
	v_lshl_add_u64 v[4:5], s[6:7], 0, v[156:157]
	s_mov_b64 s[50:51], 0
	v_ashrrev_i32_e32 v6, 4, v158
	global_load_dwordx4 v[36:39], v[2:3], off offset:2064
	global_load_dwordx4 v[32:35], v[2:3], off offset:2048
	v_mad_i64_i32 v[18:19], s[4:5], v6, s71, v[0:1]
	global_load_dwordx4 v[40:43], v[18:19], off offset:3072
	v_add_u32_e32 v9, 32, v6
	v_mad_i64_i32 v[20:21], s[4:5], v9, s71, v[0:1]
	global_load_dwordx4 v[44:47], v[20:21], off offset:3072
	v_add_u32_e32 v9, 64, v6
	v_mad_i64_i32 v[18:19], s[4:5], v9, s71, v[0:1]
	global_load_dwordx4 v[48:51], v[18:19], off offset:3072
	v_add_u32_e32 v9, 96, v6
	v_mad_i64_i32 v[20:21], s[4:5], v9, s71, v[0:1]
	global_load_dwordx4 v[52:55], v[20:21], off offset:3072
	v_lshl_add_u32 v7, v6, 8, v8
	ds_read_b128 v[22:25], v7
	s_waitcnt vmcnt(3) lgkmcnt(0)
; #define LAS __attribute__((address_space(3)))
; __device__ __forceinline__ float sigmoidf_(float x) { return 1.f / (1.f + __expf(-x)); }
; __device__ __forceinline__ unsigned pk4_fp8c(float a, float b, float c, float d) { return pk4_fp8(__builtin_amdgcn_fmed3f(a, -448.f, 448.f), __builtin_amdgcn_fmed3f(b, -448.f, 448.f), __builtin_amdgcn_fmed3f(c, -448.f, 448.f), __builtin_amdgcn_fmed3f(d, -448.f, 448.f)); }
; __device__ __forceinline__ void out_unit_m(LAS unsigned char* lds, LAS unsigned char* ldstab, const OutArgs a, const int wv) {
;     ...
;     for (int id = tid; id < 128 * 16; id += 512) { const int row = id >> 4, ch = id & 15;
;         const u32x4 y = *(const LAS u32x4*)(lds + row * TP + ch * 16); const u32x4 g = *(const u32x4*)(a.G + (size_t)row * a.ldg + 8 * ch);
;         const f32x4 g0 = *(const f32x4*)(a.gain + 8 * ch), g1 = *(const f32x4*)(a.gain + 8 * ch + 4);
;         const float yv[8] = {bf_lo(y.x), bf_hi(y.x), bf_lo(y.y), bf_hi(y.y), bf_lo(y.z), bf_hi(y.z), bf_lo(y.w), bf_hi(y.w)};
;         const float gv[8] = {bf_lo(g.x), bf_hi(g.x), bf_lo(g.y), bf_hi(g.y), bf_lo(g.z), bf_hi(g.z), bf_lo(g.w), bf_hi(g.w)};
;         const float gn[8] = {g0[0], g0[1], g0[2], g0[3], g1[0], g1[1], g1[2], g1[3]};
;         float ov[8];
; #pragma unroll
;         for (int i = 0; i < 8; ++i) ov[i] = yv[i] * gn[i] * sigmoidf_(gv[i]);
;         u32x2 w; w.x = pg8::pk4_fp8c(ov[0] * a.oscale, ov[1] * a.oscale, ov[2] * a.oscale, ov[3] * a.oscale); w.y = pg8::pk4_fp8c(ov[4] * a.oscale, ov[5] * a.oscale, ov[6] * a.oscale, ov[7] * a.oscale);
;         *(u32x2*)(a.Out + (size_t)row * a.ldo + 8 * ch) = w; }
	v_lshlrev_b32_e32 v10, 16, v22
	v_and_b32_e32 v11, 0xffff0000, v22
	v_lshlrev_b32_e32 v12, 16, v23
	v_and_b32_e32 v13, 0xffff0000, v23
	v_lshlrev_b32_e32 v14, 16, v24
	v_and_b32_e32 v15, 0xffff0000, v24
	v_lshlrev_b32_e32 v16, 16, v25
	v_and_b32_e32 v17, 0xffff0000, v25
	v_pk_mul_f32 v[10:11], v[32:33], v[10:11]
	v_pk_mul_f32 v[12:13], v[34:35], v[12:13]
	v_pk_mul_f32 v[14:15], v[36:37], v[14:15]
	v_pk_mul_f32 v[16:17], v[38:39], v[16:17]
	v_lshlrev_b32_e32 v56, 16, v40
	v_and_b32_e32 v57, 0xffff0000, v40
	v_lshlrev_b32_e32 v58, 16, v41
	v_and_b32_e32 v59, 0xffff0000, v41
	v_mul_f32_e32 v56, 0xbfb8aa3b, v56
	v_mul_f32_e32 v57, 0xbfb8aa3b, v57
	v_mul_f32_e32 v58, 0xbfb8aa3b, v58
	v_mul_f32_e32 v59, 0xbfb8aa3b, v59
	v_exp_f32_e32 v56, v56
	v_exp_f32_e32 v57, v57
	v_exp_f32_e32 v58, v58
	v_exp_f32_e32 v59, v59
	v_add_f32_e32 v56, 1.0, v56
	v_add_f32_e32 v57, 1.0, v57
	v_add_f32_e32 v58, 1.0, v58
	v_add_f32_e32 v59, 1.0, v59
	v_rcp_f32_e32 v60, v56
	v_rcp_f32_e32 v61, v57
	v_rcp_f32_e32 v62, v58
	v_rcp_f32_e32 v63, v59
	v_fma_f32 v28, -v56, v60, 1.0
	v_fma_f32 v29, -v57, v61, 1.0
	v_fma_f32 v30, -v58, v62, 1.0
	v_fma_f32 v31, -v59, v63, 1.0
	v_fmac_f32_e32 v60, v28, v60
	v_fmac_f32_e32 v61, v29, v61
	v_fmac_f32_e32 v62, v30, v62
	v_fmac_f32_e32 v63, v31, v63
	v_fma_f32 v28, -v56, v60, 1.0
	v_fma_f32 v29, -v57, v61, 1.0
	v_fma_f32 v30, -v58, v62, 1.0
	v_fma_f32 v31, -v59, v63, 1.0
	v_fma_f32 v64, v28, v60, v60
	v_fma_f32 v65, v29, v61, v61
	v_fma_f32 v66, v30, v62, v62
	v_fma_f32 v67, v31, v63, v63
	v_fma_f32 v28, -v56, v64, 1.0
	v_fma_f32 v29, -v57, v65, 1.0
	v_fma_f32 v30, -v58, v66, 1.0
	v_fma_f32 v31, -v59, v67, 1.0
	v_fma_f32 v28, v28, v60, v64
	v_fma_f32 v29, v29, v61, v65
	v_fma_f32 v30, v30, v62, v66
	v_fma_f32 v31, v31, v63, v67
	v_div_fixup_f32 v28, v28, v56, 1.0
	v_div_fixup_f32 v29, v29, v57, 1.0
	v_div_fixup_f32 v30, v30, v58, 1.0
	v_div_fixup_f32 v31, v31, v59, 1.0
	v_mul_f32_e32 v10, v10, v28
	v_mul_f32_e32 v11, v11, v29
	v_mul_f32_e32 v12, v12, v30
	v_mul_f32_e32 v13, v13, v31
	v_lshlrev_b32_e32 v56, 16, v42
	v_and_b32_e32 v57, 0xffff0000, v42
	v_lshlrev_b32_e32 v58, 16, v43
	v_and_b32_e32 v59, 0xffff0000, v43
	v_mul_f32_e32 v56, 0xbfb8aa3b, v56
	v_mul_f32_e32 v57, 0xbfb8aa3b, v57
	v_mul_f32_e32 v58, 0xbfb8aa3b, v58
	v_mul_f32_e32 v59, 0xbfb8aa3b, v59
	v_exp_f32_e32 v56, v56
	v_exp_f32_e32 v57, v57
	v_exp_f32_e32 v58, v58
	v_exp_f32_e32 v59, v59
	v_add_f32_e32 v56, 1.0, v56
	v_add_f32_e32 v57, 1.0, v57
	v_add_f32_e32 v58, 1.0, v58
	v_add_f32_e32 v59, 1.0, v59
	v_rcp_f32_e32 v60, v56
	v_rcp_f32_e32 v61, v57
	v_rcp_f32_e32 v62, v58
	v_rcp_f32_e32 v63, v59
	v_fma_f32 v28, -v56, v60, 1.0
	v_fma_f32 v29, -v57, v61, 1.0
	v_fma_f32 v30, -v58, v62, 1.0
	v_fma_f32 v31, -v59, v63, 1.0
	v_fmac_f32_e32 v60, v28, v60
	v_fmac_f32_e32 v61, v29, v61
	v_fmac_f32_e32 v62, v30, v62
	v_fmac_f32_e32 v63, v31, v63
	v_fma_f32 v28, -v56, v60, 1.0
	v_fma_f32 v29, -v57, v61, 1.0
	v_fma_f32 v30, -v58, v62, 1.0
	v_fma_f32 v31, -v59, v63, 1.0
	v_fma_f32 v64, v28, v60, v60
	v_fma_f32 v65, v29, v61, v61
	v_fma_f32 v66, v30, v62, v62
	v_fma_f32 v67, v31, v63, v63
	v_fma_f32 v28, -v56, v64, 1.0
	v_fma_f32 v29, -v57, v65, 1.0
	v_fma_f32 v30, -v58, v66, 1.0
	v_fma_f32 v31, -v59, v67, 1.0
	v_fma_f32 v28, v28, v60, v64
	v_fma_f32 v29, v29, v61, v65
	v_fma_f32 v30, v30, v62, v66
	v_fma_f32 v31, v31, v63, v67
	v_div_fixup_f32 v28, v28, v56, 1.0
	v_div_fixup_f32 v29, v29, v57, 1.0
	v_div_fixup_f32 v30, v30, v58, 1.0
	v_div_fixup_f32 v31, v31, v59, 1.0
	v_mul_f32_e32 v14, v14, v28
	v_mul_f32_e32 v15, v15, v29
	v_mul_f32_e32 v16, v16, v30
	v_mul_f32_e32 v17, v17, v31
	v_mul_f32_e32 v10, 0x41800000, v10
	v_mul_f32_e32 v11, 0x41800000, v11
	v_mul_f32_e32 v12, 0x41800000, v12
	v_mul_f32_e32 v13, 0x41800000, v13
	v_mul_f32_e32 v14, 0x41800000, v14
	v_mul_f32_e32 v15, 0x41800000, v15
	v_mul_f32_e32 v16, 0x41800000, v16
	v_mul_f32_e32 v17, 0x41800000, v17
	v_med3_f32 v10, v10, s86, v202
	v_med3_f32 v11, v11, s86, v202
	v_med3_f32 v12, v12, s86, v202
	v_med3_f32 v13, v13, s86, v202
	v_med3_f32 v14, v14, s86, v202
	v_med3_f32 v15, v15, s86, v202
	v_med3_f32 v16, v16, s86, v202
	v_med3_f32 v17, v17, s86, v202
	v_mov_b32_e32 v20, v6
	v_mov_b32_e32 v21, 0
	v_cvt_pk_fp8_f32 v26, v10, v11
	v_cvt_pk_fp8_f32 v27, v14, v15
	v_lshlrev_b64 v[20:21], 10, v[20:21]
	v_cvt_pk_fp8_f32 v26, v12, v13 op_sel:[0,0,1]
	v_cvt_pk_fp8_f32 v27, v16, v17 op_sel:[0,0,1]
	v_lshl_add_u64 v[20:21], v[4:5], 0, v[20:21]
	s_nop 0
	global_store_dwordx2 v[20:21], v[26:27], off
	v_add_u32_e32 v9, 32, v6
	v_lshl_add_u32 v7, v9, 8, v8
	ds_read_b128 v[22:25], v7
	s_waitcnt vmcnt(3) lgkmcnt(0)
; #define LAS __attribute__((address_space(3)))
; __device__ __forceinline__ float sigmoidf_(float x) { return 1.f / (1.f + __expf(-x)); }
; __device__ __forceinline__ unsigned pk4_fp8c(float a, float b, float c, float d) { return pk4_fp8(__builtin_amdgcn_fmed3f(a, -448.f, 448.f), __builtin_amdgcn_fmed3f(b, -448.f, 448.f), __builtin_amdgcn_fmed3f(c, -448.f, 448.f), __builtin_amdgcn_fmed3f(d, -448.f, 448.f)); }
; __device__ __forceinline__ void out_unit_m(LAS unsigned char* lds, LAS unsigned char* ldstab, const OutArgs a, const int wv) {
;     ...
;     for (int id = tid; id < 128 * 16; id += 512) { const int row = id >> 4, ch = id & 15;
;         const u32x4 y = *(const LAS u32x4*)(lds + row * TP + ch * 16); const u32x4 g = *(const u32x4*)(a.G + (size_t)row * a.ldg + 8 * ch);
;         const f32x4 g0 = *(const f32x4*)(a.gain + 8 * ch), g1 = *(const f32x4*)(a.gain + 8 * ch + 4);
;         const float yv[8] = {bf_lo(y.x), bf_hi(y.x), bf_lo(y.y), bf_hi(y.y), bf_lo(y.z), bf_hi(y.z), bf_lo(y.w), bf_hi(y.w)};
;         const float gv[8] = {bf_lo(g.x), bf_hi(g.x), bf_lo(g.y), bf_hi(g.y), bf_lo(g.z), bf_hi(g.z), bf_lo(g.w), bf_hi(g.w)};
;         const float gn[8] = {g0[0], g0[1], g0[2], g0[3], g1[0], g1[1], g1[2], g1[3]};
;         float ov[8];
; #pragma unroll
;         for (int i = 0; i < 8; ++i) ov[i] = yv[i] * gn[i] * sigmoidf_(gv[i]);
;         u32x2 w; w.x = pg8::pk4_fp8c(ov[0] * a.oscale, ov[1] * a.oscale, ov[2] * a.oscale, ov[3] * a.oscale); w.y = pg8::pk4_fp8c(ov[4] * a.oscale, ov[5] * a.oscale, ov[6] * a.oscale, ov[7] * a.oscale);
;         *(u32x2*)(a.Out + (size_t)row * a.ldo + 8 * ch) = w; }
	v_lshlrev_b32_e32 v10, 16, v22
	v_and_b32_e32 v11, 0xffff0000, v22
	v_lshlrev_b32_e32 v12, 16, v23
	v_and_b32_e32 v13, 0xffff0000, v23
	v_lshlrev_b32_e32 v14, 16, v24
	v_and_b32_e32 v15, 0xffff0000, v24
	v_lshlrev_b32_e32 v16, 16, v25
	v_and_b32_e32 v17, 0xffff0000, v25
	v_pk_mul_f32 v[10:11], v[32:33], v[10:11]
	v_pk_mul_f32 v[12:13], v[34:35], v[12:13]
	v_pk_mul_f32 v[14:15], v[36:37], v[14:15]
	v_pk_mul_f32 v[16:17], v[38:39], v[16:17]
	v_lshlrev_b32_e32 v56, 16, v44
	v_and_b32_e32 v57, 0xffff0000, v44
	v_lshlrev_b32_e32 v58, 16, v45
	v_and_b32_e32 v59, 0xffff0000, v45
	v_mul_f32_e32 v56, 0xbfb8aa3b, v56
	v_mul_f32_e32 v57, 0xbfb8aa3b, v57
	v_mul_f32_e32 v58, 0xbfb8aa3b, v58
	v_mul_f32_e32 v59, 0xbfb8aa3b, v59
	v_exp_f32_e32 v56, v56
	v_exp_f32_e32 v57, v57
	v_exp_f32_e32 v58, v58
	v_exp_f32_e32 v59, v59
	v_add_f32_e32 v56, 1.0, v56
	v_add_f32_e32 v57, 1.0, v57
	v_add_f32_e32 v58, 1.0, v58
	v_add_f32_e32 v59, 1.0, v59
	v_rcp_f32_e32 v60, v56
	v_rcp_f32_e32 v61, v57
	v_rcp_f32_e32 v62, v58
	v_rcp_f32_e32 v63, v59
	v_fma_f32 v28, -v56, v60, 1.0
	v_fma_f32 v29, -v57, v61, 1.0
	v_fma_f32 v30, -v58, v62, 1.0
	v_fma_f32 v31, -v59, v63, 1.0
	v_fmac_f32_e32 v60, v28, v60
	v_fmac_f32_e32 v61, v29, v61
	v_fmac_f32_e32 v62, v30, v62
	v_fmac_f32_e32 v63, v31, v63
	v_fma_f32 v28, -v56, v60, 1.0
	v_fma_f32 v29, -v57, v61, 1.0
	v_fma_f32 v30, -v58, v62, 1.0
	v_fma_f32 v31, -v59, v63, 1.0
	v_fma_f32 v64, v28, v60, v60
	v_fma_f32 v65, v29, v61, v61
	v_fma_f32 v66, v30, v62, v62
	v_fma_f32 v67, v31, v63, v63
	v_fma_f32 v28, -v56, v64, 1.0
	v_fma_f32 v29, -v57, v65, 1.0
	v_fma_f32 v30, -v58, v66, 1.0
	v_fma_f32 v31, -v59, v67, 1.0
	v_fma_f32 v28, v28, v60, v64
	v_fma_f32 v29, v29, v61, v65
	v_fma_f32 v30, v30, v62, v66
	v_fma_f32 v31, v31, v63, v67
	v_div_fixup_f32 v28, v28, v56, 1.0
	v_div_fixup_f32 v29, v29, v57, 1.0
	v_div_fixup_f32 v30, v30, v58, 1.0
	v_div_fixup_f32 v31, v31, v59, 1.0
	v_mul_f32_e32 v10, v10, v28
	v_mul_f32_e32 v11, v11, v29
	v_mul_f32_e32 v12, v12, v30
	v_mul_f32_e32 v13, v13, v31
	v_lshlrev_b32_e32 v56, 16, v46
	v_and_b32_e32 v57, 0xffff0000, v46
	v_lshlrev_b32_e32 v58, 16, v47
	v_and_b32_e32 v59, 0xffff0000, v47
	v_mul_f32_e32 v56, 0xbfb8aa3b, v56
	v_mul_f32_e32 v57, 0xbfb8aa3b, v57
	v_mul_f32_e32 v58, 0xbfb8aa3b, v58
	v_mul_f32_e32 v59, 0xbfb8aa3b, v59
	v_exp_f32_e32 v56, v56
	v_exp_f32_e32 v57, v57
	v_exp_f32_e32 v58, v58
	v_exp_f32_e32 v59, v59
	v_add_f32_e32 v56, 1.0, v56
	v_add_f32_e32 v57, 1.0, v57
	v_add_f32_e32 v58, 1.0, v58
	v_add_f32_e32 v59, 1.0, v59
	v_rcp_f32_e32 v60, v56
	v_rcp_f32_e32 v61, v57
	v_rcp_f32_e32 v62, v58
	v_rcp_f32_e32 v63, v59
	v_fma_f32 v28, -v56, v60, 1.0
	v_fma_f32 v29, -v57, v61, 1.0
	v_fma_f32 v30, -v58, v62, 1.0
	v_fma_f32 v31, -v59, v63, 1.0
	v_fmac_f32_e32 v60, v28, v60
	v_fmac_f32_e32 v61, v29, v61
	v_fmac_f32_e32 v62, v30, v62
	v_fmac_f32_e32 v63, v31, v63
	v_fma_f32 v28, -v56, v60, 1.0
	v_fma_f32 v29, -v57, v61, 1.0
	v_fma_f32 v30, -v58, v62, 1.0
	v_fma_f32 v31, -v59, v63, 1.0
	v_fma_f32 v64, v28, v60, v60
	v_fma_f32 v65, v29, v61, v61
	v_fma_f32 v66, v30, v62, v62
	v_fma_f32 v67, v31, v63, v63
	v_fma_f32 v28, -v56, v64, 1.0
	v_fma_f32 v29, -v57, v65, 1.0
	v_fma_f32 v30, -v58, v66, 1.0
	v_fma_f32 v31, -v59, v67, 1.0
	v_fma_f32 v28, v28, v60, v64
	v_fma_f32 v29, v29, v61, v65
	v_fma_f32 v30, v30, v62, v66
	v_fma_f32 v31, v31, v63, v67
	v_div_fixup_f32 v28, v28, v56, 1.0
	v_div_fixup_f32 v29, v29, v57, 1.0
	v_div_fixup_f32 v30, v30, v58, 1.0
	v_div_fixup_f32 v31, v31, v59, 1.0
	v_mul_f32_e32 v14, v14, v28
	v_mul_f32_e32 v15, v15, v29
	v_mul_f32_e32 v16, v16, v30
	v_mul_f32_e32 v17, v17, v31
	v_mul_f32_e32 v10, 0x41800000, v10
	v_mul_f32_e32 v11, 0x41800000, v11
	v_mul_f32_e32 v12, 0x41800000, v12
	v_mul_f32_e32 v13, 0x41800000, v13
	v_mul_f32_e32 v14, 0x41800000, v14
	v_mul_f32_e32 v15, 0x41800000, v15
	v_mul_f32_e32 v16, 0x41800000, v16
	v_mul_f32_e32 v17, 0x41800000, v17
	v_med3_f32 v10, v10, s86, v202
	v_med3_f32 v11, v11, s86, v202
	v_med3_f32 v12, v12, s86, v202
	v_med3_f32 v13, v13, s86, v202
	v_med3_f32 v14, v14, s86, v202
	v_med3_f32 v15, v15, s86, v202
	v_med3_f32 v16, v16, s86, v202
	v_med3_f32 v17, v17, s86, v202
	v_add_u32_e32 v20, 32, v6
	v_mov_b32_e32 v21, 0
	v_cvt_pk_fp8_f32 v26, v10, v11
	v_cvt_pk_fp8_f32 v27, v14, v15
	v_lshlrev_b64 v[20:21], 10, v[20:21]
	v_cvt_pk_fp8_f32 v26, v12, v13 op_sel:[0,0,1]
	v_cvt_pk_fp8_f32 v27, v16, v17 op_sel:[0,0,1]
	v_lshl_add_u64 v[20:21], v[4:5], 0, v[20:21]
	s_nop 0
	global_store_dwordx2 v[20:21], v[26:27], off
	v_add_u32_e32 v9, 64, v6
	v_lshl_add_u32 v7, v9, 8, v8
	ds_read_b128 v[22:25], v7
	s_waitcnt vmcnt(3) lgkmcnt(0)
; #define LAS __attribute__((address_space(3)))
; __device__ __forceinline__ float sigmoidf_(float x) { return 1.f / (1.f + __expf(-x)); }
; __device__ __forceinline__ unsigned pk4_fp8c(float a, float b, float c, float d) { return pk4_fp8(__builtin_amdgcn_fmed3f(a, -448.f, 448.f), __builtin_amdgcn_fmed3f(b, -448.f, 448.f), __builtin_amdgcn_fmed3f(c, -448.f, 448.f), __builtin_amdgcn_fmed3f(d, -448.f, 448.f)); }
; __device__ __forceinline__ void out_unit_m(LAS unsigned char* lds, LAS unsigned char* ldstab, const OutArgs a, const int wv) {
;     ...
;     for (int id = tid; id < 128 * 16; id += 512) { const int row = id >> 4, ch = id & 15;
;         const u32x4 y = *(const LAS u32x4*)(lds + row * TP + ch * 16); const u32x4 g = *(const u32x4*)(a.G + (size_t)row * a.ldg + 8 * ch);
;         const f32x4 g0 = *(const f32x4*)(a.gain + 8 * ch), g1 = *(const f32x4*)(a.gain + 8 * ch + 4);
;         const float yv[8] = {bf_lo(y.x), bf_hi(y.x), bf_lo(y.y), bf_hi(y.y), bf_lo(y.z), bf_hi(y.z), bf_lo(y.w), bf_hi(y.w)};
;         const float gv[8] = {bf_lo(g.x), bf_hi(g.x), bf_lo(g.y), bf_hi(g.y), bf_lo(g.z), bf_hi(g.z), bf_lo(g.w), bf_hi(g.w)};
;         const float gn[8] = {g0[0], g0[1], g0[2], g0[3], g1[0], g1[1], g1[2], g1[3]};
;         float ov[8];
; #pragma unroll
;         for (int i = 0; i < 8; ++i) ov[i] = yv[i] * gn[i] * sigmoidf_(gv[i]);
;         u32x2 w; w.x = pg8::pk4_fp8c(ov[0] * a.oscale, ov[1] * a.oscale, ov[2] * a.oscale, ov[3] * a.oscale); w.y = pg8::pk4_fp8c(ov[4] * a.oscale, ov[5] * a.oscale, ov[6] * a.oscale, ov[7] * a.oscale);
;         *(u32x2*)(a.Out + (size_t)row * a.ldo + 8 * ch) = w; }
	v_lshlrev_b32_e32 v10, 16, v22
	v_and_b32_e32 v11, 0xffff0000, v22
	v_lshlrev_b32_e32 v12, 16, v23
	v_and_b32_e32 v13, 0xffff0000, v23
	v_lshlrev_b32_e32 v14, 16, v24
	v_and_b32_e32 v15, 0xffff0000, v24
	v_lshlrev_b32_e32 v16, 16, v25
	v_and_b32_e32 v17, 0xffff0000, v25
	v_pk_mul_f32 v[10:11], v[32:33], v[10:11]
	v_pk_mul_f32 v[12:13], v[34:35], v[12:13]
	v_pk_mul_f32 v[14:15], v[36:37], v[14:15]
	v_pk_mul_f32 v[16:17], v[38:39], v[16:17]
	v_lshlrev_b32_e32 v56, 16, v48
	v_and_b32_e32 v57, 0xffff0000, v48
	v_lshlrev_b32_e32 v58, 16, v49
	v_and_b32_e32 v59, 0xffff0000, v49
	v_mul_f32_e32 v56, 0xbfb8aa3b, v56
	v_mul_f32_e32 v57, 0xbfb8aa3b, v57
	v_mul_f32_e32 v58, 0xbfb8aa3b, v58
	v_mul_f32_e32 v59, 0xbfb8aa3b, v59
	v_exp_f32_e32 v56, v56
	v_exp_f32_e32 v57, v57
	v_exp_f32_e32 v58, v58
	v_exp_f32_e32 v59, v59
	v_add_f32_e32 v56, 1.0, v56
	v_add_f32_e32 v57, 1.0, v57
	v_add_f32_e32 v58, 1.0, v58
	v_add_f32_e32 v59, 1.0, v59
	v_rcp_f32_e32 v60, v56
	v_rcp_f32_e32 v61, v57
	v_rcp_f32_e32 v62, v58
	v_rcp_f32_e32 v63, v59
	v_fma_f32 v28, -v56, v60, 1.0
	v_fma_f32 v29, -v57, v61, 1.0
	v_fma_f32 v30, -v58, v62, 1.0
	v_fma_f32 v31, -v59, v63, 1.0
	v_fmac_f32_e32 v60, v28, v60
	v_fmac_f32_e32 v61, v29, v61
	v_fmac_f32_e32 v62, v30, v62
	v_fmac_f32_e32 v63, v31, v63
	v_fma_f32 v28, -v56, v60, 1.0
	v_fma_f32 v29, -v57, v61, 1.0
	v_fma_f32 v30, -v58, v62, 1.0
	v_fma_f32 v31, -v59, v63, 1.0
	v_fma_f32 v64, v28, v60, v60
	v_fma_f32 v65, v29, v61, v61
	v_fma_f32 v66, v30, v62, v62
	v_fma_f32 v67, v31, v63, v63
	v_fma_f32 v28, -v56, v64, 1.0
	v_fma_f32 v29, -v57, v65, 1.0
	v_fma_f32 v30, -v58, v66, 1.0
	v_fma_f32 v31, -v59, v67, 1.0
	v_fma_f32 v28, v28, v60, v64
	v_fma_f32 v29, v29, v61, v65
	v_fma_f32 v30, v30, v62, v66
	v_fma_f32 v31, v31, v63, v67
	v_div_fixup_f32 v28, v28, v56, 1.0
	v_div_fixup_f32 v29, v29, v57, 1.0
	v_div_fixup_f32 v30, v30, v58, 1.0
	v_div_fixup_f32 v31, v31, v59, 1.0
	v_mul_f32_e32 v10, v10, v28
	v_mul_f32_e32 v11, v11, v29
	v_mul_f32_e32 v12, v12, v30
	v_mul_f32_e32 v13, v13, v31
	v_lshlrev_b32_e32 v56, 16, v50
	v_and_b32_e32 v57, 0xffff0000, v50
	v_lshlrev_b32_e32 v58, 16, v51
	v_and_b32_e32 v59, 0xffff0000, v51
	v_mul_f32_e32 v56, 0xbfb8aa3b, v56
	v_mul_f32_e32 v57, 0xbfb8aa3b, v57
	v_mul_f32_e32 v58, 0xbfb8aa3b, v58
	v_mul_f32_e32 v59, 0xbfb8aa3b, v59
	v_exp_f32_e32 v56, v56
	v_exp_f32_e32 v57, v57
	v_exp_f32_e32 v58, v58
	v_exp_f32_e32 v59, v59
	v_add_f32_e32 v56, 1.0, v56
	v_add_f32_e32 v57, 1.0, v57
	v_add_f32_e32 v58, 1.0, v58
	v_add_f32_e32 v59, 1.0, v59
	v_rcp_f32_e32 v60, v56
	v_rcp_f32_e32 v61, v57
	v_rcp_f32_e32 v62, v58
	v_rcp_f32_e32 v63, v59
	v_fma_f32 v28, -v56, v60, 1.0
	v_fma_f32 v29, -v57, v61, 1.0
	v_fma_f32 v30, -v58, v62, 1.0
	v_fma_f32 v31, -v59, v63, 1.0
	v_fmac_f32_e32 v60, v28, v60
	v_fmac_f32_e32 v61, v29, v61
	v_fmac_f32_e32 v62, v30, v62
	v_fmac_f32_e32 v63, v31, v63
	v_fma_f32 v28, -v56, v60, 1.0
	v_fma_f32 v29, -v57, v61, 1.0
	v_fma_f32 v30, -v58, v62, 1.0
	v_fma_f32 v31, -v59, v63, 1.0
	v_fma_f32 v64, v28, v60, v60
	v_fma_f32 v65, v29, v61, v61
	v_fma_f32 v66, v30, v62, v62
	v_fma_f32 v67, v31, v63, v63
	v_fma_f32 v28, -v56, v64, 1.0
	v_fma_f32 v29, -v57, v65, 1.0
	v_fma_f32 v30, -v58, v66, 1.0
	v_fma_f32 v31, -v59, v67, 1.0
	v_fma_f32 v28, v28, v60, v64
	v_fma_f32 v29, v29, v61, v65
	v_fma_f32 v30, v30, v62, v66
	v_fma_f32 v31, v31, v63, v67
	v_div_fixup_f32 v28, v28, v56, 1.0
	v_div_fixup_f32 v29, v29, v57, 1.0
	v_div_fixup_f32 v30, v30, v58, 1.0
	v_div_fixup_f32 v31, v31, v59, 1.0
	v_mul_f32_e32 v14, v14, v28
	v_mul_f32_e32 v15, v15, v29
	v_mul_f32_e32 v16, v16, v30
	v_mul_f32_e32 v17, v17, v31
	v_mul_f32_e32 v10, 0x41800000, v10
	v_mul_f32_e32 v11, 0x41800000, v11
	v_mul_f32_e32 v12, 0x41800000, v12
	v_mul_f32_e32 v13, 0x41800000, v13
	v_mul_f32_e32 v14, 0x41800000, v14
	v_mul_f32_e32 v15, 0x41800000, v15
	v_mul_f32_e32 v16, 0x41800000, v16
	v_mul_f32_e32 v17, 0x41800000, v17
	v_med3_f32 v10, v10, s86, v202
	v_med3_f32 v11, v11, s86, v202
	v_med3_f32 v12, v12, s86, v202
	v_med3_f32 v13, v13, s86, v202
	v_med3_f32 v14, v14, s86, v202
	v_med3_f32 v15, v15, s86, v202
	v_med3_f32 v16, v16, s86, v202
	v_med3_f32 v17, v17, s86, v202
	v_add_u32_e32 v20, 64, v6
	v_mov_b32_e32 v21, 0
	v_cvt_pk_fp8_f32 v26, v10, v11
	v_cvt_pk_fp8_f32 v27, v14, v15
	v_lshlrev_b64 v[20:21], 10, v[20:21]
	v_cvt_pk_fp8_f32 v26, v12, v13 op_sel:[0,0,1]
	v_cvt_pk_fp8_f32 v27, v16, v17 op_sel:[0,0,1]
	v_lshl_add_u64 v[20:21], v[4:5], 0, v[20:21]
	s_nop 0
	global_store_dwordx2 v[20:21], v[26:27], off
	v_add_u32_e32 v9, 96, v6
	v_lshl_add_u32 v7, v9, 8, v8
	ds_read_b128 v[22:25], v7
	s_waitcnt vmcnt(3) lgkmcnt(0)
; #define LAS __attribute__((address_space(3)))
; __device__ __forceinline__ float sigmoidf_(float x) { return 1.f / (1.f + __expf(-x)); }
; __device__ __forceinline__ unsigned pk4_fp8c(float a, float b, float c, float d) { return pk4_fp8(__builtin_amdgcn_fmed3f(a, -448.f, 448.f), __builtin_amdgcn_fmed3f(b, -448.f, 448.f), __builtin_amdgcn_fmed3f(c, -448.f, 448.f), __builtin_amdgcn_fmed3f(d, -448.f, 448.f)); }
; __device__ __forceinline__ void out_unit_m(LAS unsigned char* lds, LAS unsigned char* ldstab, const OutArgs a, const int wv) {
;     ...
;     for (int id = tid; id < 128 * 16; id += 512) { const int row = id >> 4, ch = id & 15;
;         const u32x4 y = *(const LAS u32x4*)(lds + row * TP + ch * 16); const u32x4 g = *(const u32x4*)(a.G + (size_t)row * a.ldg + 8 * ch);
;         const f32x4 g0 = *(const f32x4*)(a.gain + 8 * ch), g1 = *(const f32x4*)(a.gain + 8 * ch + 4);
;         const float yv[8] = {bf_lo(y.x), bf_hi(y.x), bf_lo(y.y), bf_hi(y.y), bf_lo(y.z), bf_hi(y.z), bf_lo(y.w), bf_hi(y.w)};
;         const float gv[8] = {bf_lo(g.x), bf_hi(g.x), bf_lo(g.y), bf_hi(g.y), bf_lo(g.z), bf_hi(g.z), bf_lo(g.w), bf_hi(g.w)};
;         const float gn[8] = {g0[0], g0[1], g0[2], g0[3], g1[0], g1[1], g1[2], g1[3]};
;         float ov[8];
; #pragma unroll
;         for (int i = 0; i < 8; ++i) ov[i] = yv[i] * gn[i] * sigmoidf_(gv[i]);
;         u32x2 w; w.x = pg8::pk4_fp8c(ov[0] * a.oscale, ov[1] * a.oscale, ov[2] * a.oscale, ov[3] * a.oscale); w.y = pg8::pk4_fp8c(ov[4] * a.oscale, ov[5] * a.oscale, ov[6] * a.oscale, ov[7] * a.oscale);
;         *(u32x2*)(a.Out + (size_t)row * a.ldo + 8 * ch) = w; }
	v_lshlrev_b32_e32 v10, 16, v22
	v_and_b32_e32 v11, 0xffff0000, v22
	v_lshlrev_b32_e32 v12, 16, v23
	v_and_b32_e32 v13, 0xffff0000, v23
	v_lshlrev_b32_e32 v14, 16, v24
	v_and_b32_e32 v15, 0xffff0000, v24
	v_lshlrev_b32_e32 v16, 16, v25
	v_and_b32_e32 v17, 0xffff0000, v25
	v_pk_mul_f32 v[10:11], v[32:33], v[10:11]
	v_pk_mul_f32 v[12:13], v[34:35], v[12:13]
	v_pk_mul_f32 v[14:15], v[36:37], v[14:15]
	v_pk_mul_f32 v[16:17], v[38:39], v[16:17]
	v_lshlrev_b32_e32 v56, 16, v52
	v_and_b32_e32 v57, 0xffff0000, v52
	v_lshlrev_b32_e32 v58, 16, v53
	v_and_b32_e32 v59, 0xffff0000, v53
	v_mul_f32_e32 v56, 0xbfb8aa3b, v56
	v_mul_f32_e32 v57, 0xbfb8aa3b, v57
	v_mul_f32_e32 v58, 0xbfb8aa3b, v58
	v_mul_f32_e32 v59, 0xbfb8aa3b, v59
	v_exp_f32_e32 v56, v56
	v_exp_f32_e32 v57, v57
	v_exp_f32_e32 v58, v58
	v_exp_f32_e32 v59, v59
	v_add_f32_e32 v56, 1.0, v56
	v_add_f32_e32 v57, 1.0, v57
	v_add_f32_e32 v58, 1.0, v58
	v_add_f32_e32 v59, 1.0, v59
	v_rcp_f32_e32 v60, v56
	v_rcp_f32_e32 v61, v57
	v_rcp_f32_e32 v62, v58
	v_rcp_f32_e32 v63, v59
	v_fma_f32 v28, -v56, v60, 1.0
	v_fma_f32 v29, -v57, v61, 1.0
	v_fma_f32 v30, -v58, v62, 1.0
	v_fma_f32 v31, -v59, v63, 1.0
	v_fmac_f32_e32 v60, v28, v60
	v_fmac_f32_e32 v61, v29, v61
	v_fmac_f32_e32 v62, v30, v62
	v_fmac_f32_e32 v63, v31, v63
	v_fma_f32 v28, -v56, v60, 1.0
	v_fma_f32 v29, -v57, v61, 1.0
	v_fma_f32 v30, -v58, v62, 1.0
	v_fma_f32 v31, -v59, v63, 1.0
	v_fma_f32 v64, v28, v60, v60
	v_fma_f32 v65, v29, v61, v61
	v_fma_f32 v66, v30, v62, v62
	v_fma_f32 v67, v31, v63, v63
	v_fma_f32 v28, -v56, v64, 1.0
	v_fma_f32 v29, -v57, v65, 1.0
	v_fma_f32 v30, -v58, v66, 1.0
	v_fma_f32 v31, -v59, v67, 1.0
	v_fma_f32 v28, v28, v60, v64
	v_fma_f32 v29, v29, v61, v65
	v_fma_f32 v30, v30, v62, v66
	v_fma_f32 v31, v31, v63, v67
	v_div_fixup_f32 v28, v28, v56, 1.0
	v_div_fixup_f32 v29, v29, v57, 1.0
	v_div_fixup_f32 v30, v30, v58, 1.0
	v_div_fixup_f32 v31, v31, v59, 1.0
	v_mul_f32_e32 v10, v10, v28
	v_mul_f32_e32 v11, v11, v29
	v_mul_f32_e32 v12, v12, v30
	v_mul_f32_e32 v13, v13, v31
	v_lshlrev_b32_e32 v56, 16, v54
	v_and_b32_e32 v57, 0xffff0000, v54
	v_lshlrev_b32_e32 v58, 16, v55
	v_and_b32_e32 v59, 0xffff0000, v55
	v_mul_f32_e32 v56, 0xbfb8aa3b, v56
	v_mul_f32_e32 v57, 0xbfb8aa3b, v57
	v_mul_f32_e32 v58, 0xbfb8aa3b, v58
	v_mul_f32_e32 v59, 0xbfb8aa3b, v59
	v_exp_f32_e32 v56, v56
	v_exp_f32_e32 v57, v57
	v_exp_f32_e32 v58, v58
	v_exp_f32_e32 v59, v59
	v_add_f32_e32 v56, 1.0, v56
	v_add_f32_e32 v57, 1.0, v57
	v_add_f32_e32 v58, 1.0, v58
	v_add_f32_e32 v59, 1.0, v59
	v_rcp_f32_e32 v60, v56
	v_rcp_f32_e32 v61, v57
	v_rcp_f32_e32 v62, v58
	v_rcp_f32_e32 v63, v59
	v_fma_f32 v28, -v56, v60, 1.0
	v_fma_f32 v29, -v57, v61, 1.0
	v_fma_f32 v30, -v58, v62, 1.0
	v_fma_f32 v31, -v59, v63, 1.0
	v_fmac_f32_e32 v60, v28, v60
	v_fmac_f32_e32 v61, v29, v61
	v_fmac_f32_e32 v62, v30, v62
	v_fmac_f32_e32 v63, v31, v63
	v_fma_f32 v28, -v56, v60, 1.0
	v_fma_f32 v29, -v57, v61, 1.0
	v_fma_f32 v30, -v58, v62, 1.0
	v_fma_f32 v31, -v59, v63, 1.0
	v_fma_f32 v64, v28, v60, v60
	v_fma_f32 v65, v29, v61, v61
	v_fma_f32 v66, v30, v62, v62
	v_fma_f32 v67, v31, v63, v63
	v_fma_f32 v28, -v56, v64, 1.0
	v_fma_f32 v29, -v57, v65, 1.0
	v_fma_f32 v30, -v58, v66, 1.0
	v_fma_f32 v31, -v59, v67, 1.0
	v_fma_f32 v28, v28, v60, v64
	v_fma_f32 v29, v29, v61, v65
	v_fma_f32 v30, v30, v62, v66
	v_fma_f32 v31, v31, v63, v67
	v_div_fixup_f32 v28, v28, v56, 1.0
	v_div_fixup_f32 v29, v29, v57, 1.0
	v_div_fixup_f32 v30, v30, v58, 1.0
	v_div_fixup_f32 v31, v31, v59, 1.0
	v_mul_f32_e32 v14, v14, v28
	v_mul_f32_e32 v15, v15, v29
	v_mul_f32_e32 v16, v16, v30
	v_mul_f32_e32 v17, v17, v31
	v_mul_f32_e32 v10, 0x41800000, v10
	v_mul_f32_e32 v11, 0x41800000, v11
	v_mul_f32_e32 v12, 0x41800000, v12
	v_mul_f32_e32 v13, 0x41800000, v13
	v_mul_f32_e32 v14, 0x41800000, v14
	v_mul_f32_e32 v15, 0x41800000, v15
	v_mul_f32_e32 v16, 0x41800000, v16
	v_mul_f32_e32 v17, 0x41800000, v17
	v_med3_f32 v10, v10, s86, v202
	v_med3_f32 v11, v11, s86, v202
	v_med3_f32 v12, v12, s86, v202
	v_med3_f32 v13, v13, s86, v202
	v_med3_f32 v14, v14, s86, v202
	v_med3_f32 v15, v15, s86, v202
	v_med3_f32 v16, v16, s86, v202
	v_med3_f32 v17, v17, s86, v202
	v_add_u32_e32 v20, 96, v6
	v_mov_b32_e32 v21, 0
	v_cvt_pk_fp8_f32 v26, v10, v11
	v_cvt_pk_fp8_f32 v27, v14, v15
	v_lshlrev_b64 v[20:21], 10, v[20:21]
	v_cvt_pk_fp8_f32 v26, v12, v13 op_sel:[0,0,1]
	v_cvt_pk_fp8_f32 v27, v16, v17 op_sel:[0,0,1]
	v_lshl_add_u64 v[20:21], v[4:5], 0, v[20:21]
	s_nop 0
	global_store_dwordx2 v[20:21], v[26:27], off
